# v_AA plus 46 LDS-DMA loads of the P2/P10/P12/P15 K-loops in SGPR-base + 32-bit VGPR-offset form (dead 64-bit VALU address adds removed)
# baseline (speedup 1.0000x reference)
.LBB0_318:
	ds_read_b128 v[26:29], v185
	ds_read_b128 v[30:33], v185 offset:1024
	ds_read_b128 v[18:21], v185 offset:2048
	ds_read_b128 v[22:25], v185 offset:3072
	ds_read_b128 v[10:13], v186
	ds_read_b128 v[14:17], v186 offset:1024
	ds_read_b128 v[2:5], v186 offset:2048
	ds_read_b128 v[6:9], v186 offset:3072
	s_add_u32 s24, s26, 0xffea8080
	s_addc_u32 s25, s27, -1
	s_cmpk_eq_i32 s58, 0x52
	s_cselect_b32 s31, s5, s25
	s_cselect_b32 s30, s4, s24
	s_cselect_b32 s29, s21, s51
	s_cselect_b32 s28, s20, s50
	s_add_i32 m0, s7, 0xc000
	ds_read_b128 v[174:177], v187
	ds_read_b128 v[178:181], v187 offset:1024
	ds_read_b128 v[188:191], v187 offset:2048
	ds_read_b128 v[192:195], v187 offset:3072
	ds_read_b128 v[196:199], v187 offset:4096
	ds_read_b128 v[200:203], v187 offset:5120
	ds_read_b128 v[204:207], v187 offset:6144
	ds_read_b128 v[208:211], v187 offset:7168
	global_load_lds_dwordx4 v166, s[26:27]
	v_lshl_add_u64 v[212:213], s[26:27], 0, v[168:169]
	s_add_i32 m0, s7, 0xe000
	s_nop 0
	global_load_lds_dwordx4 v[212:213], off
	s_waitcnt vmcnt(8) lgkmcnt(0)
	s_barrier
	s_setprio 1
	v_mfma_f32_16x16x128_f8f6f4 v[158:161], v[26:33], v[174:181], v[158:161]
	v_mfma_f32_16x16x128_f8f6f4 v[154:157], v[18:25], v[174:181], v[154:157]
	v_mfma_f32_16x16x128_f8f6f4 v[138:141], v[18:25], v[188:195], v[138:141]
	v_mfma_f32_16x16x128_f8f6f4 v[142:145], v[26:33], v[188:195], v[142:145]
	v_mfma_f32_16x16x128_f8f6f4 v[126:129], v[26:33], v[196:203], v[126:129]
	v_mfma_f32_16x16x128_f8f6f4 v[122:125], v[18:25], v[196:203], v[122:125]
	v_mfma_f32_16x16x128_f8f6f4 v[106:109], v[18:25], v[204:211], v[106:109]
	v_mfma_f32_16x16x128_f8f6f4 v[110:113], v[26:33], v[204:211], v[110:113]
	v_mfma_f32_16x16x128_f8f6f4 v[102:105], v[10:17], v[204:211], v[102:105]
	v_mfma_f32_16x16x128_f8f6f4 v[98:101], v[2:9], v[204:211], v[98:101]
	v_mfma_f32_16x16x128_f8f6f4 v[146:149], v[2:9], v[174:181], v[146:149]
	v_mfma_f32_16x16x128_f8f6f4 v[150:153], v[10:17], v[174:181], v[150:153]
	v_mfma_f32_16x16x128_f8f6f4 v[134:137], v[10:17], v[188:195], v[134:137]
	v_mfma_f32_16x16x128_f8f6f4 v[130:133], v[2:9], v[188:195], v[130:133]
	v_mfma_f32_16x16x128_f8f6f4 v[114:117], v[2:9], v[196:203], v[114:117]
	v_mfma_f32_16x16x128_f8f6f4 v[118:121], v[10:17], v[196:203], v[118:121]
	s_setprio 0
	s_barrier
	s_add_i32 s24, s42, s3
	v_lshl_add_u64 v[174:175], s[28:29], 0, v[164:165]
	s_mov_b32 m0, s24
	ds_read_b128 v[188:191], v187 offset:16384
	ds_read_b128 v[192:195], v187 offset:17408
	ds_read_b128 v[196:199], v187 offset:18432
	ds_read_b128 v[200:203], v187 offset:19456
	ds_read_b128 v[204:207], v187 offset:20480
	ds_read_b128 v[208:211], v187 offset:21504
	ds_read_b128 v[212:215], v187 offset:22528
	ds_read_b128 v[216:219], v187 offset:23552
	global_load_lds_dwordx4 v[174:175], off
	s_add_i32 m0, s24, 0x2000
	s_add_u32 s24, s28, 0x158000
	v_lshl_add_u64 v[176:177], s[28:29], 0, v[162:163]
	s_addc_u32 s25, s29, 0
	s_add_i32 s59, s43, s3
	global_load_lds_dwordx4 v[176:177], off
	s_mov_b32 m0, s59
	v_lshl_add_u64 v[180:181], s[30:31], 0, v[162:163]
	global_load_lds_dwordx4 v164, s[24:25]
	s_add_i32 m0, s59, 0x2000
	s_nop 0
	global_load_lds_dwordx4 v162, s[24:25]
	v_lshl_add_u64 v[178:179], s[30:31], 0, v[164:165]
	s_mov_b32 m0, s7
	s_nop 0
	global_load_lds_dwordx4 v[178:179], off
	s_mov_b32 m0, s17
	s_nop 0
	global_load_lds_dwordx4 v[180:181], off
	s_waitcnt vmcnt(8) lgkmcnt(0)
	s_barrier
	s_setprio 1
	v_mfma_f32_16x16x128_f8f6f4 v[78:81], v[26:33], v[196:203], v[78:81]
	v_mfma_f32_16x16x128_f8f6f4 v[74:77], v[18:25], v[196:203], v[74:77]
	v_mfma_f32_16x16x128_f8f6f4 v[90:93], v[18:25], v[188:195], v[90:93]
	v_mfma_f32_16x16x128_f8f6f4 v[94:97], v[26:33], v[188:195], v[94:97]
	v_mfma_f32_16x16x128_f8f6f4 v[62:65], v[26:33], v[204:211], v[62:65]
	v_mfma_f32_16x16x128_f8f6f4 v[58:61], v[18:25], v[204:211], v[58:61]
	v_mfma_f32_16x16x128_f8f6f4 v[42:45], v[18:25], v[212:219], v[42:45]
	v_mfma_f32_16x16x128_f8f6f4 v[46:49], v[26:33], v[212:219], v[46:49]
	v_mfma_f32_16x16x128_f8f6f4 v[38:41], v[10:17], v[212:219], v[38:41]
	v_mfma_f32_16x16x128_f8f6f4 v[34:37], v[2:9], v[212:219], v[34:37]
	v_mfma_f32_16x16x128_f8f6f4 v[82:85], v[2:9], v[188:195], v[82:85]
	v_mfma_f32_16x16x128_f8f6f4 v[86:89], v[10:17], v[188:195], v[86:89]
	v_mfma_f32_16x16x128_f8f6f4 v[70:73], v[10:17], v[196:203], v[70:73]
	v_mfma_f32_16x16x128_f8f6f4 v[66:69], v[2:9], v[196:203], v[66:69]
	v_mfma_f32_16x16x128_f8f6f4 v[50:53], v[2:9], v[204:211], v[50:53]
	v_mfma_f32_16x16x128_f8f6f4 v[54:57], v[10:17], v[204:211], v[54:57]
	s_setprio 0
	s_barrier
	s_add_i32 s59, 0, 0x18000
	s_add_i32 s60, 0, 0x1c000
	v_add_u32_e32 v14, s59, v183
	v_add_u32_e32 v30, s60, v183
	ds_read_b128 v[2:5], v14
	ds_read_b128 v[6:9], v14 offset:1024
	ds_read_b128 v[10:13], v14 offset:2048
	ds_read_b128 v[14:17], v14 offset:3072
	ds_read_b128 v[18:21], v30
	ds_read_b128 v[22:25], v30 offset:1024
	ds_read_b128 v[26:29], v30 offset:2048
	ds_read_b128 v[30:33], v30 offset:3072
	s_add_u32 s24, s30, 0x158000
	s_addc_u32 s25, s31, 0
	s_mov_b32 m0, s34
	ds_read_b128 v[188:191], v187 offset:32768
	ds_read_b128 v[192:195], v187 offset:33792
	ds_read_b128 v[196:199], v187 offset:34816
	ds_read_b128 v[200:203], v187 offset:35840
	ds_read_b128 v[204:207], v187 offset:36864
	ds_read_b128 v[208:211], v187 offset:37888
	ds_read_b128 v[212:215], v187 offset:38912
	ds_read_b128 v[216:219], v187 offset:39936
	global_load_lds_dwordx4 v164, s[24:25]
	s_mov_b32 m0, s35
	s_nop 0
	global_load_lds_dwordx4 v162, s[24:25]
	s_waitcnt vmcnt(8) lgkmcnt(0)
	s_barrier
	s_setprio 1
	v_mfma_f32_16x16x128_f8f6f4 v[122:125], v[10:17], v[204:211], v[122:125]
	v_mfma_f32_16x16x128_f8f6f4 v[126:129], v[2:9], v[204:211], v[126:129]
	v_mfma_f32_16x16x128_f8f6f4 v[158:161], v[2:9], v[188:195], v[158:161]
	v_mfma_f32_16x16x128_f8f6f4 v[154:157], v[10:17], v[188:195], v[154:157]
	v_mfma_f32_16x16x128_f8f6f4 v[138:141], v[10:17], v[196:203], v[138:141]
	v_mfma_f32_16x16x128_f8f6f4 v[142:145], v[2:9], v[196:203], v[142:145]
	v_mfma_f32_16x16x128_f8f6f4 v[110:113], v[2:9], v[212:219], v[110:113]
	v_mfma_f32_16x16x128_f8f6f4 v[106:109], v[10:17], v[212:219], v[106:109]
	v_mfma_f32_16x16x128_f8f6f4 v[102:105], v[18:25], v[212:219], v[102:105]
	v_mfma_f32_16x16x128_f8f6f4 v[98:101], v[26:33], v[212:219], v[98:101]
	v_mfma_f32_16x16x128_f8f6f4 v[146:149], v[26:33], v[188:195], v[146:149]
	v_mfma_f32_16x16x128_f8f6f4 v[150:153], v[18:25], v[188:195], v[150:153]
	v_mfma_f32_16x16x128_f8f6f4 v[134:137], v[18:25], v[196:203], v[134:137]
	v_mfma_f32_16x16x128_f8f6f4 v[130:133], v[26:33], v[196:203], v[130:133]
	v_mfma_f32_16x16x128_f8f6f4 v[114:117], v[26:33], v[204:211], v[114:117]
	v_mfma_f32_16x16x128_f8f6f4 v[118:121], v[18:25], v[204:211], v[118:121]
	s_setprio 0
	s_barrier
	s_add_i32 s24, s59, s3
	v_lshl_add_u64 v[174:175], v[174:175], 0, s[12:13]
	s_mov_b32 m0, s24
	ds_read_b128 v[188:191], v187 offset:49152
	ds_read_b128 v[192:195], v187 offset:50176
	ds_read_b128 v[196:199], v187 offset:51200
	ds_read_b128 v[200:203], v187 offset:52224
	ds_read_b128 v[204:207], v187 offset:53248
	ds_read_b128 v[208:211], v187 offset:54272
	ds_read_b128 v[212:215], v187 offset:55296
	ds_read_b128 v[216:219], v187 offset:56320
	global_load_lds_dwordx4 v[174:175], off
	s_add_i32 m0, s24, 0x2000
	s_add_u32 s24, s28, 0x158080
	v_lshl_add_u64 v[174:175], v[176:177], 0, s[12:13]
	s_addc_u32 s25, s29, 0
	s_add_i32 s28, s60, s3
	global_load_lds_dwordx4 v[174:175], off
	s_mov_b32 m0, s28
	s_nop 0
	global_load_lds_dwordx4 v164, s[24:25]
	s_add_i32 m0, s28, 0x2000
	s_nop 0
	global_load_lds_dwordx4 v162, s[24:25]
	v_lshl_add_u64 v[174:175], v[178:179], 0, s[12:13]
	s_mov_b32 m0, s38
	s_nop 0
	global_load_lds_dwordx4 v[174:175], off
	v_lshl_add_u64 v[174:175], v[180:181], 0, s[12:13]
	s_mov_b32 m0, s39
	s_nop 0
	global_load_lds_dwordx4 v[174:175], off
	s_waitcnt vmcnt(8) lgkmcnt(0)
	s_barrier
	s_setprio 1
	v_mfma_f32_16x16x128_f8f6f4 v[62:65], v[2:9], v[204:211], v[62:65]
	v_mfma_f32_16x16x128_f8f6f4 v[58:61], v[10:17], v[204:211], v[58:61]
	v_mfma_f32_16x16x128_f8f6f4 v[90:93], v[10:17], v[188:195], v[90:93]
	v_mfma_f32_16x16x128_f8f6f4 v[94:97], v[2:9], v[188:195], v[94:97]
	v_mfma_f32_16x16x128_f8f6f4 v[78:81], v[2:9], v[196:203], v[78:81]
	v_mfma_f32_16x16x128_f8f6f4 v[74:77], v[10:17], v[196:203], v[74:77]
	v_mfma_f32_16x16x128_f8f6f4 v[42:45], v[10:17], v[212:219], v[42:45]
	v_mfma_f32_16x16x128_f8f6f4 v[46:49], v[2:9], v[212:219], v[46:49]
	v_mfma_f32_16x16x128_f8f6f4 v[38:41], v[18:25], v[212:219], v[38:41]
	v_mfma_f32_16x16x128_f8f6f4 v[34:37], v[26:33], v[212:219], v[34:37]
	v_mfma_f32_16x16x128_f8f6f4 v[82:85], v[26:33], v[188:195], v[82:85]
	v_mfma_f32_16x16x128_f8f6f4 v[86:89], v[18:25], v[188:195], v[86:89]
	v_mfma_f32_16x16x128_f8f6f4 v[70:73], v[18:25], v[196:203], v[70:73]
	v_mfma_f32_16x16x128_f8f6f4 v[66:69], v[26:33], v[196:203], v[66:69]
	v_mfma_f32_16x16x128_f8f6f4 v[50:53], v[26:33], v[204:211], v[50:53]
	v_mfma_f32_16x16x128_f8f6f4 v[54:57], v[18:25], v[204:211], v[54:57]
	s_setprio 0
	s_barrier
	s_add_i32 s58, s58, 2
	s_add_u32 s26, s26, 0x100
	s_addc_u32 s27, s27, 0
	s_add_u32 s50, s50, 0x100
	s_addc_u32 s51, s51, 0
	s_cmpk_gt_u32 s58, 0x53
	s_cbranch_scc0 .LBB0_318
	s_and_b64 vcc, exec, s[14:15]
	s_cbranch_vccz .LBB0_321
	s_barrier

.LBB0_332:
	s_add_u32 s6, s61, s4
	s_addc_u32 s7, s62, s5
	s_add_u32 s6, s6, 0x32800100
	s_addc_u32 s7, s7, 0
	s_add_u32 s24, s63, s4
	s_addc_u32 s25, s68, s5
	s_add_i32 s64, 0, 0x10000
	s_cmpk_eq_i32 s4, 0x2a00
	s_cselect_b32 s13, s1, s7
	s_cselect_b32 s12, s0, s6
	s_cselect_b32 s7, s29, s25
	s_cselect_b32 s6, s28, s24
	s_add_i32 s65, 0, 0x14000
	v_add_u32_e32 v2, s64, v188
	v_add_u32_e32 v6, s65, v188
	ds_read_b128 v[26:29], v2
	ds_read_b128 v[30:33], v2 offset:1024
	ds_read_b128 v[18:21], v2 offset:2048
	ds_read_b128 v[22:25], v2 offset:3072
	ds_read_b128 v[10:13], v6
	ds_read_b128 v[14:17], v6 offset:1024
	ds_read_b128 v[2:5], v6 offset:2048
	ds_read_b128 v[6:9], v6 offset:3072
	v_lshl_add_u64 v[214:215], v[168:169], 0, s[4:5]
	s_add_i32 m0, s18, 0xc000
	ds_read_b128 v[172:175], v189
	ds_read_b128 v[176:179], v189 offset:1024
	ds_read_b128 v[190:193], v189 offset:2048
	ds_read_b128 v[194:197], v189 offset:3072
	ds_read_b128 v[198:201], v189 offset:4096
	ds_read_b128 v[202:205], v189 offset:5120
	ds_read_b128 v[206:209], v189 offset:6144
	ds_read_b128 v[210:213], v189 offset:7168
	global_load_lds_dwordx4 v[214:215], off
	v_lshl_add_u64 v[214:215], v[170:171], 0, s[4:5]
	s_add_i32 m0, s18, 0xe000
	s_nop 0
	global_load_lds_dwordx4 v[214:215], off
	s_waitcnt vmcnt(8) lgkmcnt(0)
	s_barrier
	s_setprio 1
	v_mfma_f32_16x16x128_f8f6f4 v[70:73], v[26:33], v[172:179], v[70:73]
	v_mfma_f32_16x16x128_f8f6f4 v[66:69], v[18:25], v[172:179], v[66:69]
	v_mfma_f32_16x16x128_f8f6f4 v[74:77], v[18:25], v[190:197], v[74:77]
	v_mfma_f32_16x16x128_f8f6f4 v[78:81], v[26:33], v[190:197], v[78:81]
	v_mfma_f32_16x16x128_f8f6f4 v[86:89], v[26:33], v[198:205], v[86:89]
	v_mfma_f32_16x16x128_f8f6f4 v[82:85], v[18:25], v[198:205], v[82:85]
	v_mfma_f32_16x16x128_f8f6f4 v[90:93], v[18:25], v[206:213], v[90:93]
	v_mfma_f32_16x16x128_f8f6f4 v[94:97], v[26:33], v[206:213], v[94:97]
	v_mfma_f32_16x16x128_f8f6f4 v[134:137], v[10:17], v[206:213], v[134:137]
	v_mfma_f32_16x16x128_f8f6f4 v[130:133], v[2:9], v[206:213], v[130:133]
	v_mfma_f32_16x16x128_f8f6f4 v[154:157], v[2:9], v[172:179], v[154:157]
	v_mfma_f32_16x16x128_f8f6f4 v[158:161], v[10:17], v[172:179], v[158:161]
	v_mfma_f32_16x16x128_f8f6f4 v[150:153], v[10:17], v[190:197], v[150:153]
	v_mfma_f32_16x16x128_f8f6f4 v[146:149], v[2:9], v[190:197], v[146:149]
	v_mfma_f32_16x16x128_f8f6f4 v[138:141], v[2:9], v[198:205], v[138:141]
	v_mfma_f32_16x16x128_f8f6f4 v[142:145], v[10:17], v[198:205], v[142:145]
	s_setprio 0
	s_barrier
	s_add_i32 s24, s64, s17
	v_lshl_add_u64 v[172:173], s[6:7], 0, v[162:163]
	s_mov_b32 m0, s24
	ds_read_b128 v[190:193], v189 offset:16384
	ds_read_b128 v[194:197], v189 offset:17408
	ds_read_b128 v[198:201], v189 offset:18432
	ds_read_b128 v[202:205], v189 offset:19456
	ds_read_b128 v[206:209], v189 offset:20480
	ds_read_b128 v[210:213], v189 offset:21504
	ds_read_b128 v[214:217], v189 offset:22528
	ds_read_b128 v[218:221], v189 offset:23552
	global_load_lds_dwordx4 v[172:173], off
	s_add_i32 m0, s24, 0x2000
	s_add_u32 s24, s6, 0x158000
	v_lshl_add_u64 v[174:175], s[6:7], 0, v[166:167]
	s_addc_u32 s25, s7, 0
	s_add_i32 s64, s65, s17
	global_load_lds_dwordx4 v[174:175], off
	s_mov_b32 m0, s64
	v_lshl_add_u64 v[178:179], s[12:13], 0, v[166:167]
	global_load_lds_dwordx4 v162, s[24:25]
	s_add_i32 m0, s64, 0x2000
	s_nop 0
	global_load_lds_dwordx4 v166, s[24:25]
	v_lshl_add_u64 v[176:177], s[12:13], 0, v[162:163]
	s_mov_b32 m0, s18
	s_nop 0
	global_load_lds_dwordx4 v[176:177], off
	s_mov_b32 m0, s19
	s_nop 0
	global_load_lds_dwordx4 v[178:179], off
	s_waitcnt vmcnt(8) lgkmcnt(0)
	s_barrier
	s_setprio 1
	v_mfma_f32_16x16x128_f8f6f4 v[110:113], v[26:33], v[198:205], v[110:113]
	v_mfma_f32_16x16x128_f8f6f4 v[106:109], v[18:25], v[198:205], v[106:109]
	v_mfma_f32_16x16x128_f8f6f4 v[98:101], v[18:25], v[190:197], v[98:101]
	v_mfma_f32_16x16x128_f8f6f4 v[102:105], v[26:33], v[190:197], v[102:105]
	v_mfma_f32_16x16x128_f8f6f4 v[118:121], v[26:33], v[206:213], v[118:121]
	v_mfma_f32_16x16x128_f8f6f4 v[114:117], v[18:25], v[206:213], v[114:117]
	v_mfma_f32_16x16x128_f8f6f4 v[122:125], v[18:25], v[214:221], v[122:125]
	v_mfma_f32_16x16x128_f8f6f4 v[126:129], v[26:33], v[214:221], v[126:129]
	v_mfma_f32_16x16x128_f8f6f4 v[62:65], v[10:17], v[214:221], v[62:65]
	v_mfma_f32_16x16x128_f8f6f4 v[58:61], v[2:9], v[214:221], v[58:61]
	v_mfma_f32_16x16x128_f8f6f4 v[34:37], v[2:9], v[190:197], v[34:37]
	v_mfma_f32_16x16x128_f8f6f4 v[38:41], v[10:17], v[190:197], v[38:41]
	v_mfma_f32_16x16x128_f8f6f4 v[46:49], v[10:17], v[198:205], v[46:49]
	v_mfma_f32_16x16x128_f8f6f4 v[42:45], v[2:9], v[198:205], v[42:45]
	v_mfma_f32_16x16x128_f8f6f4 v[50:53], v[2:9], v[206:213], v[50:53]
	v_mfma_f32_16x16x128_f8f6f4 v[54:57], v[10:17], v[206:213], v[54:57]
	s_setprio 0
	s_barrier
	s_add_i32 s24, 0, 0x18000
	s_add_i32 s25, 0, 0x1c000
	v_add_u32_e32 v14, s24, v188
	v_add_u32_e32 v30, s25, v188
	ds_read_b128 v[2:5], v14
	ds_read_b128 v[6:9], v14 offset:1024
	ds_read_b128 v[10:13], v14 offset:2048
	ds_read_b128 v[14:17], v14 offset:3072
	ds_read_b128 v[18:21], v30
	ds_read_b128 v[22:25], v30 offset:1024
	ds_read_b128 v[26:29], v30 offset:2048
	ds_read_b128 v[30:33], v30 offset:3072
	s_add_u32 s12, s12, 0x158000
	s_addc_u32 s13, s13, 0
	s_mov_b32 m0, s93
	ds_read_b128 v[190:193], v189 offset:32768
	ds_read_b128 v[194:197], v189 offset:33792
	ds_read_b128 v[198:201], v189 offset:34816
	ds_read_b128 v[202:205], v189 offset:35840
	ds_read_b128 v[206:209], v189 offset:36864
	ds_read_b128 v[210:213], v189 offset:37888
	ds_read_b128 v[214:217], v189 offset:38912
	ds_read_b128 v[218:221], v189 offset:39936
	global_load_lds_dwordx4 v162, s[12:13]
	s_mov_b32 m0, s94
	s_nop 0
	global_load_lds_dwordx4 v166, s[12:13]
	s_waitcnt vmcnt(8) lgkmcnt(0)
	s_barrier
	s_setprio 1
	v_mfma_f32_16x16x128_f8f6f4 v[82:85], v[10:17], v[206:213], v[82:85]
	v_mfma_f32_16x16x128_f8f6f4 v[86:89], v[2:9], v[206:213], v[86:89]
	v_mfma_f32_16x16x128_f8f6f4 v[70:73], v[2:9], v[190:197], v[70:73]
	v_mfma_f32_16x16x128_f8f6f4 v[66:69], v[10:17], v[190:197], v[66:69]
	v_mfma_f32_16x16x128_f8f6f4 v[74:77], v[10:17], v[198:205], v[74:77]
	v_mfma_f32_16x16x128_f8f6f4 v[78:81], v[2:9], v[198:205], v[78:81]
	v_mfma_f32_16x16x128_f8f6f4 v[94:97], v[2:9], v[214:221], v[94:97]
	v_mfma_f32_16x16x128_f8f6f4 v[90:93], v[10:17], v[214:221], v[90:93]
	v_mfma_f32_16x16x128_f8f6f4 v[134:137], v[18:25], v[214:221], v[134:137]
	v_mfma_f32_16x16x128_f8f6f4 v[130:133], v[26:33], v[214:221], v[130:133]
	v_mfma_f32_16x16x128_f8f6f4 v[154:157], v[26:33], v[190:197], v[154:157]
	v_mfma_f32_16x16x128_f8f6f4 v[158:161], v[18:25], v[190:197], v[158:161]
	v_mfma_f32_16x16x128_f8f6f4 v[150:153], v[18:25], v[198:205], v[150:153]
	v_mfma_f32_16x16x128_f8f6f4 v[146:149], v[26:33], v[198:205], v[146:149]
	v_mfma_f32_16x16x128_f8f6f4 v[138:141], v[26:33], v[206:213], v[138:141]
	v_mfma_f32_16x16x128_f8f6f4 v[142:145], v[18:25], v[206:213], v[142:145]
	s_setprio 0
	s_barrier
	s_add_i32 s12, s24, s17
	v_lshl_add_u64 v[172:173], v[172:173], 0, s[76:77]
	s_mov_b32 m0, s12
	ds_read_b128 v[190:193], v189 offset:49152
	ds_read_b128 v[194:197], v189 offset:50176
	ds_read_b128 v[198:201], v189 offset:51200
	ds_read_b128 v[202:205], v189 offset:52224
	ds_read_b128 v[206:209], v189 offset:53248
	ds_read_b128 v[210:213], v189 offset:54272
	ds_read_b128 v[214:217], v189 offset:55296
	ds_read_b128 v[218:221], v189 offset:56320
	global_load_lds_dwordx4 v[172:173], off
	s_add_i32 m0, s12, 0x2000
	s_add_u32 s6, s6, 0x158080
	v_lshl_add_u64 v[172:173], v[174:175], 0, s[76:77]
	s_addc_u32 s7, s7, 0
	s_add_i32 s12, s25, s17
	global_load_lds_dwordx4 v[172:173], off
	s_mov_b32 m0, s12
	s_nop 0
	global_load_lds_dwordx4 v162, s[6:7]
	s_add_i32 m0, s12, 0x2000
	s_nop 0
	global_load_lds_dwordx4 v166, s[6:7]
	v_lshl_add_u64 v[172:173], v[176:177], 0, s[76:77]
	s_mov_b32 m0, s95
	s_nop 0
	global_load_lds_dwordx4 v[172:173], off
	v_lshl_add_u64 v[172:173], v[178:179], 0, s[76:77]
	s_mov_b32 m0, vcc_lo
	s_nop 0
	global_load_lds_dwordx4 v[172:173], off
	s_waitcnt vmcnt(8) lgkmcnt(0)
	s_barrier
	s_setprio 1
	v_mfma_f32_16x16x128_f8f6f4 v[118:121], v[2:9], v[206:213], v[118:121]
	v_mfma_f32_16x16x128_f8f6f4 v[114:117], v[10:17], v[206:213], v[114:117]
	v_mfma_f32_16x16x128_f8f6f4 v[98:101], v[10:17], v[190:197], v[98:101]
	v_mfma_f32_16x16x128_f8f6f4 v[102:105], v[2:9], v[190:197], v[102:105]
	v_mfma_f32_16x16x128_f8f6f4 v[110:113], v[2:9], v[198:205], v[110:113]
	v_mfma_f32_16x16x128_f8f6f4 v[106:109], v[10:17], v[198:205], v[106:109]
	v_mfma_f32_16x16x128_f8f6f4 v[122:125], v[10:17], v[214:221], v[122:125]
	v_mfma_f32_16x16x128_f8f6f4 v[126:129], v[2:9], v[214:221], v[126:129]
	v_mfma_f32_16x16x128_f8f6f4 v[62:65], v[18:25], v[214:221], v[62:65]
	v_mfma_f32_16x16x128_f8f6f4 v[58:61], v[26:33], v[214:221], v[58:61]
	v_mfma_f32_16x16x128_f8f6f4 v[34:37], v[26:33], v[190:197], v[34:37]
	v_mfma_f32_16x16x128_f8f6f4 v[38:41], v[18:25], v[190:197], v[38:41]
	v_mfma_f32_16x16x128_f8f6f4 v[46:49], v[18:25], v[198:205], v[46:49]
	v_mfma_f32_16x16x128_f8f6f4 v[42:45], v[26:33], v[198:205], v[42:45]
	v_mfma_f32_16x16x128_f8f6f4 v[50:53], v[26:33], v[206:213], v[50:53]
	v_mfma_f32_16x16x128_f8f6f4 v[54:57], v[18:25], v[206:213], v[54:57]
	s_setprio 0
	s_barrier
	s_add_i32 vcc_hi, vcc_hi, 2
	s_add_u32 s4, s4, 0x100
	s_addc_u32 s5, s5, 0
	s_cmpk_lt_u32 vcc_hi, 0x54
	s_cbranch_scc1 .LBB0_332
	s_waitcnt vmcnt(0)
	s_mov_b64 s[12:13], s[54:55]
	s_cmpk_gt_u32 s89, 0xff
	s_cbranch_scc1 .LBB0_335
	s_barrier

.LBB0_1291:
	ds_read_b128 v[26:29], v184
	ds_read_b128 v[30:33], v184 offset:1024
	ds_read_b128 v[18:21], v184 offset:2048
	ds_read_b128 v[22:25], v184 offset:3072
	ds_read_b128 v[10:13], v185
	ds_read_b128 v[14:17], v185 offset:1024
	ds_read_b128 v[2:5], v185 offset:2048
	ds_read_b128 v[6:9], v185 offset:3072
	s_add_u32 s20, s14, s16
	s_addc_u32 s21, s15, s17
	s_add_u32 s20, s20, 0x2a800100
	s_addc_u32 s21, s21, 0
	s_add_u32 s48, s31, s16
	s_addc_u32 s49, s34, s17
	s_cmpk_eq_i32 s16, 0x700
	s_cselect_b32 s23, s9, s21
	s_cselect_b32 s22, s8, s20
	s_cselect_b32 s21, s5, s49
	s_cselect_b32 s20, s4, s48
	s_mov_b32 m0, s36
	v_lshl_add_u64 v[214:215], v[170:171], 0, s[16:17]
	ds_read_b128 v[174:177], v186
	ds_read_b128 v[178:181], v186 offset:1024
	ds_read_b128 v[190:193], v186 offset:2048
	ds_read_b128 v[194:197], v186 offset:3072
	ds_read_b128 v[198:201], v186 offset:4096
	ds_read_b128 v[202:205], v186 offset:5120
	ds_read_b128 v[206:209], v186 offset:6144
	ds_read_b128 v[210:213], v186 offset:7168
	global_load_lds_dwordx4 v[214:215], off
	v_lshl_add_u64 v[214:215], v[172:173], 0, s[16:17]
	s_mov_b32 m0, s37
	s_nop 0
	global_load_lds_dwordx4 v[214:215], off
	s_waitcnt vmcnt(8) lgkmcnt(0)
	s_barrier
	s_setprio 1
	v_mfma_f32_16x16x128_f8f6f4 v[158:161], v[26:33], v[174:181], v[158:161]
	v_mfma_f32_16x16x128_f8f6f4 v[154:157], v[18:25], v[174:181], v[154:157]
	v_mfma_f32_16x16x128_f8f6f4 v[138:141], v[18:25], v[190:197], v[138:141]
	v_mfma_f32_16x16x128_f8f6f4 v[146:149], v[26:33], v[190:197], v[146:149]
	v_mfma_f32_16x16x128_f8f6f4 v[130:133], v[26:33], v[198:205], v[130:133]
	v_mfma_f32_16x16x128_f8f6f4 v[122:125], v[18:25], v[198:205], v[122:125]
	v_mfma_f32_16x16x128_f8f6f4 v[106:109], v[18:25], v[206:213], v[106:109]
	v_mfma_f32_16x16x128_f8f6f4 v[114:117], v[26:33], v[206:213], v[114:117]
	v_mfma_f32_16x16x128_f8f6f4 v[102:105], v[10:17], v[206:213], v[102:105]
	v_mfma_f32_16x16x128_f8f6f4 v[98:101], v[2:9], v[206:213], v[98:101]
	v_mfma_f32_16x16x128_f8f6f4 v[142:145], v[2:9], v[174:181], v[142:145]
	v_mfma_f32_16x16x128_f8f6f4 v[150:153], v[10:17], v[174:181], v[150:153]
	v_mfma_f32_16x16x128_f8f6f4 v[134:137], v[10:17], v[190:197], v[134:137]
	v_mfma_f32_16x16x128_f8f6f4 v[126:129], v[2:9], v[190:197], v[126:129]
	v_mfma_f32_16x16x128_f8f6f4 v[110:113], v[2:9], v[198:205], v[110:113]
	v_mfma_f32_16x16x128_f8f6f4 v[118:121], v[10:17], v[198:205], v[118:121]
	s_setprio 0
	s_barrier
	s_mov_b32 m0, s38
	v_lshl_add_u64 v[174:175], s[20:21], 0, v[164:165]
	s_add_u32 s48, s20, 0x80000
	ds_read_b128 v[190:193], v186 offset:16384
	ds_read_b128 v[194:197], v186 offset:17408
	ds_read_b128 v[198:201], v186 offset:18432
	ds_read_b128 v[202:205], v186 offset:19456
	ds_read_b128 v[206:209], v186 offset:20480
	ds_read_b128 v[210:213], v186 offset:21504
	ds_read_b128 v[214:217], v186 offset:22528
	ds_read_b128 v[218:221], v186 offset:23552
	global_load_lds_dwordx4 v[174:175], off
	v_lshl_add_u64 v[176:177], s[20:21], 0, v[168:169]
	s_mov_b32 m0, s39
	s_addc_u32 s49, s21, 0
	global_load_lds_dwordx4 v[176:177], off
	s_mov_b32 m0, s40
	v_lshl_add_u64 v[180:181], s[22:23], 0, v[166:167]
	global_load_lds_dwordx4 v164, s[48:49]
	s_mov_b32 m0, s41
	s_nop 0
	global_load_lds_dwordx4 v168, s[48:49]
	v_lshl_add_u64 v[178:179], s[22:23], 0, v[162:163]
	s_mov_b32 m0, s24
	s_nop 0
	global_load_lds_dwordx4 v[178:179], off
	s_mov_b32 m0, s25
	s_nop 0
	global_load_lds_dwordx4 v[180:181], off
	s_waitcnt vmcnt(8) lgkmcnt(0)
	s_barrier
	s_setprio 1
	v_mfma_f32_16x16x128_f8f6f4 v[82:85], v[26:33], v[198:205], v[82:85]
	v_mfma_f32_16x16x128_f8f6f4 v[74:77], v[18:25], v[198:205], v[74:77]
	v_mfma_f32_16x16x128_f8f6f4 v[90:93], v[18:25], v[190:197], v[90:93]
	v_mfma_f32_16x16x128_f8f6f4 v[94:97], v[26:33], v[190:197], v[94:97]
	v_mfma_f32_16x16x128_f8f6f4 v[66:69], v[26:33], v[206:213], v[66:69]
	v_mfma_f32_16x16x128_f8f6f4 v[58:61], v[18:25], v[206:213], v[58:61]
	v_mfma_f32_16x16x128_f8f6f4 v[42:45], v[18:25], v[214:221], v[42:45]
	v_mfma_f32_16x16x128_f8f6f4 v[50:53], v[26:33], v[214:221], v[50:53]
	v_mfma_f32_16x16x128_f8f6f4 v[38:41], v[10:17], v[214:221], v[38:41]
	v_mfma_f32_16x16x128_f8f6f4 v[34:37], v[2:9], v[214:221], v[34:37]
	v_mfma_f32_16x16x128_f8f6f4 v[78:81], v[2:9], v[190:197], v[78:81]
	v_mfma_f32_16x16x128_f8f6f4 v[86:89], v[10:17], v[190:197], v[86:89]
	v_mfma_f32_16x16x128_f8f6f4 v[70:73], v[10:17], v[198:205], v[70:73]
	v_mfma_f32_16x16x128_f8f6f4 v[62:65], v[2:9], v[198:205], v[62:65]
	v_mfma_f32_16x16x128_f8f6f4 v[46:49], v[2:9], v[206:213], v[46:49]
	v_mfma_f32_16x16x128_f8f6f4 v[54:57], v[10:17], v[206:213], v[54:57]
	s_setprio 0
	s_barrier
	ds_read_b128 v[2:5], v187
	ds_read_b128 v[6:9], v187 offset:1024
	ds_read_b128 v[10:13], v187 offset:2048
	ds_read_b128 v[14:17], v187 offset:3072
	ds_read_b128 v[18:21], v188
	ds_read_b128 v[22:25], v188 offset:1024
	ds_read_b128 v[26:29], v188 offset:2048
	ds_read_b128 v[30:33], v188 offset:3072
	s_add_u32 s22, s22, 0x80000
	s_addc_u32 s23, s23, 0
	s_mov_b32 m0, s26
	ds_read_b128 v[190:193], v186 offset:32768
	ds_read_b128 v[194:197], v186 offset:33792
	ds_read_b128 v[198:201], v186 offset:34816
	ds_read_b128 v[202:205], v186 offset:35840
	ds_read_b128 v[206:209], v186 offset:36864
	ds_read_b128 v[210:213], v186 offset:37888
	ds_read_b128 v[214:217], v186 offset:38912
	ds_read_b128 v[218:221], v186 offset:39936
	global_load_lds_dwordx4 v162, s[22:23]
	s_mov_b32 m0, s27
	s_nop 0
	global_load_lds_dwordx4 v166, s[22:23]
	s_waitcnt vmcnt(8) lgkmcnt(0)
	s_barrier
	s_setprio 1
	v_mfma_f32_16x16x128_f8f6f4 v[122:125], v[10:17], v[206:213], v[122:125]
	v_mfma_f32_16x16x128_f8f6f4 v[130:133], v[2:9], v[206:213], v[130:133]
	v_mfma_f32_16x16x128_f8f6f4 v[158:161], v[2:9], v[190:197], v[158:161]
	v_mfma_f32_16x16x128_f8f6f4 v[154:157], v[10:17], v[190:197], v[154:157]
	v_mfma_f32_16x16x128_f8f6f4 v[138:141], v[10:17], v[198:205], v[138:141]
	v_mfma_f32_16x16x128_f8f6f4 v[146:149], v[2:9], v[198:205], v[146:149]
	v_mfma_f32_16x16x128_f8f6f4 v[114:117], v[2:9], v[214:221], v[114:117]
	v_mfma_f32_16x16x128_f8f6f4 v[106:109], v[10:17], v[214:221], v[106:109]
	v_mfma_f32_16x16x128_f8f6f4 v[102:105], v[18:25], v[214:221], v[102:105]
	v_mfma_f32_16x16x128_f8f6f4 v[98:101], v[26:33], v[214:221], v[98:101]
	v_mfma_f32_16x16x128_f8f6f4 v[142:145], v[26:33], v[190:197], v[142:145]
	v_mfma_f32_16x16x128_f8f6f4 v[150:153], v[18:25], v[190:197], v[150:153]
	v_mfma_f32_16x16x128_f8f6f4 v[134:137], v[18:25], v[198:205], v[134:137]
	v_mfma_f32_16x16x128_f8f6f4 v[126:129], v[26:33], v[198:205], v[126:129]
	v_mfma_f32_16x16x128_f8f6f4 v[110:113], v[26:33], v[206:213], v[110:113]
	v_mfma_f32_16x16x128_f8f6f4 v[118:121], v[18:25], v[206:213], v[118:121]
	s_setprio 0
	s_barrier
	s_mov_b32 m0, s42
	v_lshl_add_u64 v[174:175], v[174:175], 0, s[12:13]
	s_add_u32 s20, s20, 0x80080
	ds_read_b128 v[190:193], v186 offset:49152
	ds_read_b128 v[194:197], v186 offset:50176
	ds_read_b128 v[198:201], v186 offset:51200
	ds_read_b128 v[202:205], v186 offset:52224
	ds_read_b128 v[206:209], v186 offset:53248
	ds_read_b128 v[210:213], v186 offset:54272
	ds_read_b128 v[214:217], v186 offset:55296
	ds_read_b128 v[218:221], v186 offset:56320
	global_load_lds_dwordx4 v[174:175], off
	v_lshl_add_u64 v[174:175], v[176:177], 0, s[12:13]
	s_mov_b32 m0, s43
	s_addc_u32 s21, s21, 0
	global_load_lds_dwordx4 v[174:175], off
	s_mov_b32 m0, s44
	s_nop 0
	global_load_lds_dwordx4 v164, s[20:21]
	s_mov_b32 m0, s45
	s_nop 0
	global_load_lds_dwordx4 v168, s[20:21]
	v_lshl_add_u64 v[174:175], v[178:179], 0, s[12:13]
	s_mov_b32 m0, s29
	s_nop 0
	global_load_lds_dwordx4 v[174:175], off
	v_lshl_add_u64 v[174:175], v[180:181], 0, s[12:13]
	s_mov_b32 m0, s30
	s_nop 0
	global_load_lds_dwordx4 v[174:175], off
	s_waitcnt vmcnt(8) lgkmcnt(0)
	s_barrier
	s_setprio 1
	v_mfma_f32_16x16x128_f8f6f4 v[66:69], v[2:9], v[206:213], v[66:69]
	v_mfma_f32_16x16x128_f8f6f4 v[58:61], v[10:17], v[206:213], v[58:61]
	v_mfma_f32_16x16x128_f8f6f4 v[90:93], v[10:17], v[190:197], v[90:93]
	v_mfma_f32_16x16x128_f8f6f4 v[94:97], v[2:9], v[190:197], v[94:97]
	v_mfma_f32_16x16x128_f8f6f4 v[82:85], v[2:9], v[198:205], v[82:85]
	v_mfma_f32_16x16x128_f8f6f4 v[74:77], v[10:17], v[198:205], v[74:77]
	v_mfma_f32_16x16x128_f8f6f4 v[42:45], v[10:17], v[214:221], v[42:45]
	v_mfma_f32_16x16x128_f8f6f4 v[50:53], v[2:9], v[214:221], v[50:53]
	v_mfma_f32_16x16x128_f8f6f4 v[38:41], v[18:25], v[214:221], v[38:41]
	v_mfma_f32_16x16x128_f8f6f4 v[34:37], v[26:33], v[214:221], v[34:37]
	v_mfma_f32_16x16x128_f8f6f4 v[78:81], v[26:33], v[190:197], v[78:81]
	v_mfma_f32_16x16x128_f8f6f4 v[86:89], v[18:25], v[190:197], v[86:89]
	v_mfma_f32_16x16x128_f8f6f4 v[70:73], v[18:25], v[198:205], v[70:73]
	v_mfma_f32_16x16x128_f8f6f4 v[62:65], v[26:33], v[198:205], v[62:65]
	v_mfma_f32_16x16x128_f8f6f4 v[46:49], v[26:33], v[206:213], v[46:49]
	v_mfma_f32_16x16x128_f8f6f4 v[54:57], v[18:25], v[206:213], v[54:57]
	s_setprio 0
	s_barrier
	s_add_i32 s35, s35, 2
	s_add_u32 s16, s16, 0x100
	s_addc_u32 s17, s17, 0
	s_cmp_gt_u32 s35, 13
	s_cbranch_scc0 .LBB0_1291
	s_cmpk_lt_u32 s19, 0x100
	s_cbranch_scc0 .LBB0_1294
	s_barrier

.LBB0_1309:
	ds_read_b128 v[26:29], v189
	ds_read_b128 v[30:33], v189 offset:1024
	ds_read_b128 v[18:21], v189 offset:2048
	ds_read_b128 v[22:25], v189 offset:3072
	ds_read_b128 v[10:13], v190
	ds_read_b128 v[14:17], v190 offset:1024
	ds_read_b128 v[2:5], v190 offset:2048
	ds_read_b128 v[6:9], v190 offset:3072
	s_add_u32 s40, s38, 0xfff80080
	s_addc_u32 s41, s39, -1
	s_cmp_eq_u32 s72, 28
	s_cselect_b32 s43, s18, s41
	s_cselect_b32 s42, s19, s40
	s_cselect_b32 s41, s27, s71
	s_cselect_b32 s40, s29, s70
	s_add_i32 m0, s37, 0xc000
	ds_read_b128 v[178:181], v191
	ds_read_b128 v[182:185], v191 offset:1024
	ds_read_b128 v[192:195], v191 offset:2048
	ds_read_b128 v[196:199], v191 offset:3072
	ds_read_b128 v[200:203], v191 offset:4096
	ds_read_b128 v[204:207], v191 offset:5120
	ds_read_b128 v[208:211], v191 offset:6144
	ds_read_b128 v[212:215], v191 offset:7168
	global_load_lds_dwordx4 v170, s[38:39]
	v_lshl_add_u64 v[216:217], s[38:39], 0, v[172:173]
	s_add_i32 m0, s37, 0xe000
	s_nop 0
	global_load_lds_dwordx4 v[216:217], off
	s_waitcnt vmcnt(8) lgkmcnt(0)
	s_barrier
	s_setprio 1
	v_mfma_f32_16x16x128_f8f6f4 v[158:161], v[26:33], v[178:185], v[158:161]
	v_mfma_f32_16x16x128_f8f6f4 v[154:157], v[18:25], v[178:185], v[154:157]
	v_mfma_f32_16x16x128_f8f6f4 v[138:141], v[18:25], v[192:199], v[138:141]
	v_mfma_f32_16x16x128_f8f6f4 v[146:149], v[26:33], v[192:199], v[146:149]
	v_mfma_f32_16x16x128_f8f6f4 v[130:133], v[26:33], v[200:207], v[130:133]
	v_mfma_f32_16x16x128_f8f6f4 v[122:125], v[18:25], v[200:207], v[122:125]
	v_mfma_f32_16x16x128_f8f6f4 v[106:109], v[18:25], v[208:215], v[106:109]
	v_mfma_f32_16x16x128_f8f6f4 v[114:117], v[26:33], v[208:215], v[114:117]
	v_mfma_f32_16x16x128_f8f6f4 v[102:105], v[10:17], v[208:215], v[102:105]
	v_mfma_f32_16x16x128_f8f6f4 v[98:101], v[2:9], v[208:215], v[98:101]
	v_mfma_f32_16x16x128_f8f6f4 v[142:145], v[2:9], v[178:185], v[142:145]
	v_mfma_f32_16x16x128_f8f6f4 v[150:153], v[10:17], v[178:185], v[150:153]
	v_mfma_f32_16x16x128_f8f6f4 v[134:137], v[10:17], v[192:199], v[134:137]
	v_mfma_f32_16x16x128_f8f6f4 v[126:129], v[2:9], v[192:199], v[126:129]
	v_mfma_f32_16x16x128_f8f6f4 v[110:113], v[2:9], v[200:207], v[110:113]
	v_mfma_f32_16x16x128_f8f6f4 v[118:121], v[10:17], v[200:207], v[118:121]
	s_setprio 0
	s_barrier
	s_add_i32 s64, s59, s3
	v_lshl_add_u64 v[178:179], s[40:41], 0, v[166:167]
	s_mov_b32 m0, s64
	ds_read_b128 v[192:195], v191 offset:16384
	ds_read_b128 v[196:199], v191 offset:17408
	ds_read_b128 v[200:203], v191 offset:18432
	ds_read_b128 v[204:207], v191 offset:19456
	ds_read_b128 v[208:211], v191 offset:20480
	ds_read_b128 v[212:215], v191 offset:21504
	ds_read_b128 v[216:219], v191 offset:22528
	ds_read_b128 v[220:223], v191 offset:23552
	global_load_lds_dwordx4 v[178:179], off
	s_add_i32 m0, s64, 0x2000
	s_add_u32 s64, s40, 0x80000
	v_lshl_add_u64 v[180:181], s[40:41], 0, v[162:163]
	s_addc_u32 s65, s41, 0
	s_add_i32 s73, s62, s3
	global_load_lds_dwordx4 v[180:181], off
	s_mov_b32 m0, s73
	v_lshl_add_u64 v[184:185], s[42:43], 0, v[164:165]
	global_load_lds_dwordx4 v166, s[64:65]
	s_add_i32 m0, s73, 0x2000
	s_nop 0
	global_load_lds_dwordx4 v162, s[64:65]
	v_lshl_add_u64 v[182:183], s[42:43], 0, v[168:169]
	s_mov_b32 m0, s37
	s_nop 0
	global_load_lds_dwordx4 v[182:183], off
	s_mov_b32 m0, s44
	s_nop 0
	global_load_lds_dwordx4 v[184:185], off
	s_waitcnt vmcnt(8) lgkmcnt(0)
	s_barrier
	s_setprio 1
	v_mfma_f32_16x16x128_f8f6f4 v[82:85], v[26:33], v[200:207], v[82:85]
	v_mfma_f32_16x16x128_f8f6f4 v[74:77], v[18:25], v[200:207], v[74:77]
	v_mfma_f32_16x16x128_f8f6f4 v[90:93], v[18:25], v[192:199], v[90:93]
	v_mfma_f32_16x16x128_f8f6f4 v[94:97], v[26:33], v[192:199], v[94:97]
	v_mfma_f32_16x16x128_f8f6f4 v[66:69], v[26:33], v[208:215], v[66:69]
	v_mfma_f32_16x16x128_f8f6f4 v[58:61], v[18:25], v[208:215], v[58:61]
	v_mfma_f32_16x16x128_f8f6f4 v[42:45], v[18:25], v[216:223], v[42:45]
	v_mfma_f32_16x16x128_f8f6f4 v[50:53], v[26:33], v[216:223], v[50:53]
	v_mfma_f32_16x16x128_f8f6f4 v[38:41], v[10:17], v[216:223], v[38:41]
	v_mfma_f32_16x16x128_f8f6f4 v[34:37], v[2:9], v[216:223], v[34:37]
	v_mfma_f32_16x16x128_f8f6f4 v[78:81], v[2:9], v[192:199], v[78:81]
	v_mfma_f32_16x16x128_f8f6f4 v[86:89], v[10:17], v[192:199], v[86:89]
	v_mfma_f32_16x16x128_f8f6f4 v[70:73], v[10:17], v[200:207], v[70:73]
	v_mfma_f32_16x16x128_f8f6f4 v[62:65], v[2:9], v[200:207], v[62:65]
	v_mfma_f32_16x16x128_f8f6f4 v[46:49], v[2:9], v[208:215], v[46:49]
	v_mfma_f32_16x16x128_f8f6f4 v[54:57], v[10:17], v[208:215], v[54:57]
	s_setprio 0
	s_barrier
	s_add_i32 s64, 0, 0x18000
	s_add_i32 s65, 0, 0x1c000
	v_add_u32_e32 v14, s64, v187
	v_add_u32_e32 v30, s65, v187
	ds_read_b128 v[2:5], v14
	ds_read_b128 v[6:9], v14 offset:1024
	ds_read_b128 v[10:13], v14 offset:2048
	ds_read_b128 v[14:17], v14 offset:3072
	ds_read_b128 v[18:21], v30
	ds_read_b128 v[22:25], v30 offset:1024
	ds_read_b128 v[26:29], v30 offset:2048
	ds_read_b128 v[30:33], v30 offset:3072
	s_add_u32 s42, s42, 0x80000
	s_addc_u32 s43, s43, 0
	s_mov_b32 m0, s45
	ds_read_b128 v[192:195], v191 offset:32768
	ds_read_b128 v[196:199], v191 offset:33792
	ds_read_b128 v[200:203], v191 offset:34816
	ds_read_b128 v[204:207], v191 offset:35840
	ds_read_b128 v[208:211], v191 offset:36864
	ds_read_b128 v[212:215], v191 offset:37888
	ds_read_b128 v[216:219], v191 offset:38912
	ds_read_b128 v[220:223], v191 offset:39936
	global_load_lds_dwordx4 v168, s[42:43]
	s_mov_b32 m0, s48
	s_nop 0
	global_load_lds_dwordx4 v164, s[42:43]
	s_waitcnt vmcnt(8) lgkmcnt(0)
	s_barrier
	s_setprio 1
	v_mfma_f32_16x16x128_f8f6f4 v[122:125], v[10:17], v[208:215], v[122:125]
	v_mfma_f32_16x16x128_f8f6f4 v[130:133], v[2:9], v[208:215], v[130:133]
	v_mfma_f32_16x16x128_f8f6f4 v[158:161], v[2:9], v[192:199], v[158:161]
	v_mfma_f32_16x16x128_f8f6f4 v[154:157], v[10:17], v[192:199], v[154:157]
	v_mfma_f32_16x16x128_f8f6f4 v[138:141], v[10:17], v[200:207], v[138:141]
	v_mfma_f32_16x16x128_f8f6f4 v[146:149], v[2:9], v[200:207], v[146:149]
	v_mfma_f32_16x16x128_f8f6f4 v[114:117], v[2:9], v[216:223], v[114:117]
	v_mfma_f32_16x16x128_f8f6f4 v[106:109], v[10:17], v[216:223], v[106:109]
	v_mfma_f32_16x16x128_f8f6f4 v[102:105], v[18:25], v[216:223], v[102:105]
	v_mfma_f32_16x16x128_f8f6f4 v[98:101], v[26:33], v[216:223], v[98:101]
	v_mfma_f32_16x16x128_f8f6f4 v[142:145], v[26:33], v[192:199], v[142:145]
	v_mfma_f32_16x16x128_f8f6f4 v[150:153], v[18:25], v[192:199], v[150:153]
	v_mfma_f32_16x16x128_f8f6f4 v[134:137], v[18:25], v[200:207], v[134:137]
	v_mfma_f32_16x16x128_f8f6f4 v[126:129], v[26:33], v[200:207], v[126:129]
	v_mfma_f32_16x16x128_f8f6f4 v[110:113], v[26:33], v[208:215], v[110:113]
	v_mfma_f32_16x16x128_f8f6f4 v[118:121], v[18:25], v[208:215], v[118:121]
	s_setprio 0
	s_barrier
	s_add_i32 s42, s64, s3
	v_lshl_add_u64 v[178:179], v[178:179], 0, s[12:13]
	s_mov_b32 m0, s42
	ds_read_b128 v[192:195], v191 offset:49152
	ds_read_b128 v[196:199], v191 offset:50176
	ds_read_b128 v[200:203], v191 offset:51200
	ds_read_b128 v[204:207], v191 offset:52224
	ds_read_b128 v[208:211], v191 offset:53248
	ds_read_b128 v[212:215], v191 offset:54272
	ds_read_b128 v[216:219], v191 offset:55296
	ds_read_b128 v[220:223], v191 offset:56320
	global_load_lds_dwordx4 v[178:179], off
	s_add_i32 m0, s42, 0x2000
	s_add_u32 s40, s40, 0x80080
	v_lshl_add_u64 v[178:179], v[180:181], 0, s[12:13]
	s_addc_u32 s41, s41, 0
	s_add_i32 s42, s65, s3
	global_load_lds_dwordx4 v[178:179], off
	s_mov_b32 m0, s42
	s_nop 0
	global_load_lds_dwordx4 v166, s[40:41]
	s_add_i32 m0, s42, 0x2000
	s_nop 0
	global_load_lds_dwordx4 v162, s[40:41]
	v_lshl_add_u64 v[178:179], v[182:183], 0, s[12:13]
	s_mov_b32 m0, s51
	s_nop 0
	global_load_lds_dwordx4 v[178:179], off
	v_lshl_add_u64 v[178:179], v[184:185], 0, s[12:13]
	s_mov_b32 m0, s58
	s_nop 0
	global_load_lds_dwordx4 v[178:179], off
	s_waitcnt vmcnt(8) lgkmcnt(0)
	s_barrier
	s_setprio 1
	v_mfma_f32_16x16x128_f8f6f4 v[66:69], v[2:9], v[208:215], v[66:69]
	v_mfma_f32_16x16x128_f8f6f4 v[58:61], v[10:17], v[208:215], v[58:61]
	v_mfma_f32_16x16x128_f8f6f4 v[90:93], v[10:17], v[192:199], v[90:93]
	v_mfma_f32_16x16x128_f8f6f4 v[94:97], v[2:9], v[192:199], v[94:97]
	v_mfma_f32_16x16x128_f8f6f4 v[82:85], v[2:9], v[200:207], v[82:85]
	v_mfma_f32_16x16x128_f8f6f4 v[74:77], v[10:17], v[200:207], v[74:77]
	v_mfma_f32_16x16x128_f8f6f4 v[42:45], v[10:17], v[216:223], v[42:45]
	v_mfma_f32_16x16x128_f8f6f4 v[50:53], v[2:9], v[216:223], v[50:53]
	v_mfma_f32_16x16x128_f8f6f4 v[38:41], v[18:25], v[216:223], v[38:41]
	v_mfma_f32_16x16x128_f8f6f4 v[34:37], v[26:33], v[216:223], v[34:37]
	v_mfma_f32_16x16x128_f8f6f4 v[78:81], v[26:33], v[192:199], v[78:81]
	v_mfma_f32_16x16x128_f8f6f4 v[86:89], v[18:25], v[192:199], v[86:89]
	v_mfma_f32_16x16x128_f8f6f4 v[70:73], v[18:25], v[200:207], v[70:73]
	v_mfma_f32_16x16x128_f8f6f4 v[62:65], v[26:33], v[200:207], v[62:65]
	v_mfma_f32_16x16x128_f8f6f4 v[46:49], v[26:33], v[208:215], v[46:49]
	v_mfma_f32_16x16x128_f8f6f4 v[54:57], v[18:25], v[208:215], v[54:57]
	s_setprio 0
	s_barrier
	s_add_i32 s72, s72, 2
	s_add_u32 s38, s38, 0x100
	s_addc_u32 s39, s39, 0
	s_add_u32 s70, s70, 0x100
	s_addc_u32 s71, s71, 0
	s_cmp_gt_u32 s72, 29
	s_cbranch_scc0 .LBB0_1309
	s_and_b64 vcc, exec, s[14:15]
	s_cbranch_vccz .LBB0_1312
	s_barrier

.LBB0_1558:
	s_add_u32 s39, s30, s38
	s_addc_u32 s44, s31, 0
	s_add_u32 s42, s39, 0x100
	s_addc_u32 s43, s44, 0
	s_and_b64 s[40:41], s[36:37], exec
	s_cselect_b32 s41, s18, s43
	s_cselect_b32 s40, s19, s42
	s_add_u32 s38, s28, s38
	s_addc_u32 s42, s29, 0
	s_add_u32 s38, s38, 0x100
	s_addc_u32 s42, s42, 0
	s_and_b64 s[36:37], s[36:37], exec
	s_cselect_b32 s43, s17, s42
	s_cselect_b32 s42, s21, s38
	s_add_u32 s76, s39, 0x10080
	ds_read_b128 v[26:29], v181
	ds_read_b128 v[30:33], v181 offset:1024
	ds_read_b128 v[18:21], v181 offset:2048
	ds_read_b128 v[22:25], v181 offset:3072
	ds_read_b128 v[10:13], v182
	ds_read_b128 v[14:17], v182 offset:1024
	ds_read_b128 v[2:5], v182 offset:2048
	ds_read_b128 v[6:9], v182 offset:3072
	s_addc_u32 s77, s44, 0
	s_add_i32 s75, s63, s15
	s_add_i32 m0, s27, 0xc000
	s_add_i32 s78, s27, 0xe000
	s_add_i32 s72, s75, 0x2000
	s_add_u32 s44, s42, 0x10000
	s_addc_u32 s45, s43, 0
	s_add_i32 s74, s64, s15
	s_add_i32 s73, s74, 0x2000
	s_add_i32 s71, 0, 0x18000
	s_add_i32 s70, 0, 0x1c000
	s_add_u32 s38, s40, 0x10000
	s_addc_u32 s39, s41, 0
	s_add_i32 s69, s71, s15
	s_add_i32 s67, s69, 0x2000
	s_add_u32 s36, s42, 0x10080
	s_addc_u32 s37, s43, 0
	s_add_i32 s68, s70, s15
	s_add_i32 s66, s68, 0x2000
	ds_read_b128 v[170:173], v183
	ds_read_b128 v[174:177], v183 offset:1024
	ds_read_b128 v[184:187], v183 offset:2048
	ds_read_b128 v[188:191], v183 offset:3072
	ds_read_b128 v[192:195], v183 offset:4096
	ds_read_b128 v[196:199], v183 offset:5120
	ds_read_b128 v[200:203], v183 offset:6144
	ds_read_b128 v[204:207], v183 offset:7168
	global_load_lds_dwordx4 v164, s[76:77]
	v_lshl_add_u64 v[208:209], s[76:77], 0, v[162:163]
	s_mov_b32 m0, s78
	s_nop 0
	global_load_lds_dwordx4 v[208:209], off
	s_waitcnt vmcnt(8) lgkmcnt(0)
	s_barrier
	s_setprio 1
	v_mfma_f32_16x16x128_f8f6f4 v[158:161], v[26:33], v[170:177], v[158:161]
	v_mfma_f32_16x16x128_f8f6f4 v[154:157], v[18:25], v[170:177], v[154:157]
	v_mfma_f32_16x16x128_f8f6f4 v[138:141], v[18:25], v[184:191], v[138:141]
	v_mfma_f32_16x16x128_f8f6f4 v[142:145], v[26:33], v[184:191], v[142:145]
	v_mfma_f32_16x16x128_f8f6f4 v[126:129], v[26:33], v[192:199], v[126:129]
	v_mfma_f32_16x16x128_f8f6f4 v[122:125], v[18:25], v[192:199], v[122:125]
	v_mfma_f32_16x16x128_f8f6f4 v[106:109], v[18:25], v[200:207], v[106:109]
	v_mfma_f32_16x16x128_f8f6f4 v[110:113], v[26:33], v[200:207], v[110:113]
	v_mfma_f32_16x16x128_f8f6f4 v[102:105], v[10:17], v[200:207], v[102:105]
	v_mfma_f32_16x16x128_f8f6f4 v[98:101], v[2:9], v[200:207], v[98:101]
	v_mfma_f32_16x16x128_f8f6f4 v[146:149], v[2:9], v[170:177], v[146:149]
	v_mfma_f32_16x16x128_f8f6f4 v[150:153], v[10:17], v[170:177], v[150:153]
	v_mfma_f32_16x16x128_f8f6f4 v[134:137], v[10:17], v[184:191], v[134:137]
	v_mfma_f32_16x16x128_f8f6f4 v[130:133], v[2:9], v[184:191], v[130:133]
	v_mfma_f32_16x16x128_f8f6f4 v[114:117], v[2:9], v[192:199], v[114:117]
	v_mfma_f32_16x16x128_f8f6f4 v[118:121], v[10:17], v[192:199], v[118:121]
	s_setprio 0
	s_barrier
	s_mov_b32 m0, s75
	v_lshl_add_u64 v[170:171], s[42:43], 0, v[164:165]
	ds_read_b128 v[184:187], v183 offset:16384
	ds_read_b128 v[188:191], v183 offset:17408
	ds_read_b128 v[192:195], v183 offset:18432
	ds_read_b128 v[196:199], v183 offset:19456
	ds_read_b128 v[200:203], v183 offset:20480
	ds_read_b128 v[204:207], v183 offset:21504
	ds_read_b128 v[208:211], v183 offset:22528
	ds_read_b128 v[212:215], v183 offset:23552
	global_load_lds_dwordx4 v[170:171], off
	v_lshl_add_u64 v[172:173], s[42:43], 0, v[162:163]
	s_mov_b32 m0, s72
	global_load_lds_dwordx4 v[172:173], off
	s_mov_b32 m0, s74
	v_lshl_add_u64 v[176:177], s[40:41], 0, v[162:163]
	global_load_lds_dwordx4 v164, s[44:45]
	s_mov_b32 m0, s73
	s_nop 0
	global_load_lds_dwordx4 v162, s[44:45]
	v_lshl_add_u64 v[174:175], s[40:41], 0, v[164:165]
	s_mov_b32 m0, s27
	s_nop 0
	global_load_lds_dwordx4 v[174:175], off
	s_mov_b32 m0, s49
	s_nop 0
	global_load_lds_dwordx4 v[176:177], off
	s_waitcnt vmcnt(8) lgkmcnt(0)
	s_barrier
	s_setprio 1
	v_mfma_f32_16x16x128_f8f6f4 v[78:81], v[26:33], v[192:199], v[78:81]
	v_mfma_f32_16x16x128_f8f6f4 v[74:77], v[18:25], v[192:199], v[74:77]
	v_mfma_f32_16x16x128_f8f6f4 v[90:93], v[18:25], v[184:191], v[90:93]
	v_mfma_f32_16x16x128_f8f6f4 v[94:97], v[26:33], v[184:191], v[94:97]
	v_mfma_f32_16x16x128_f8f6f4 v[62:65], v[26:33], v[200:207], v[62:65]
	v_mfma_f32_16x16x128_f8f6f4 v[58:61], v[18:25], v[200:207], v[58:61]
	v_mfma_f32_16x16x128_f8f6f4 v[42:45], v[18:25], v[208:215], v[42:45]
	v_mfma_f32_16x16x128_f8f6f4 v[54:57], v[26:33], v[208:215], v[54:57]
	v_mfma_f32_16x16x128_f8f6f4 v[38:41], v[10:17], v[208:215], v[38:41]
	v_mfma_f32_16x16x128_f8f6f4 v[34:37], v[2:9], v[208:215], v[34:37]
	v_mfma_f32_16x16x128_f8f6f4 v[82:85], v[2:9], v[184:191], v[82:85]
	v_mfma_f32_16x16x128_f8f6f4 v[86:89], v[10:17], v[184:191], v[86:89]
	v_mfma_f32_16x16x128_f8f6f4 v[70:73], v[10:17], v[192:199], v[70:73]
	v_mfma_f32_16x16x128_f8f6f4 v[66:69], v[2:9], v[192:199], v[66:69]
	v_mfma_f32_16x16x128_f8f6f4 v[46:49], v[2:9], v[200:207], v[46:49]
	v_mfma_f32_16x16x128_f8f6f4 v[50:53], v[10:17], v[200:207], v[50:53]
	s_setprio 0
	s_barrier
	v_add_u32_e32 v14, s71, v179
	v_add_u32_e32 v30, s70, v179
	ds_read_b128 v[2:5], v14
	ds_read_b128 v[6:9], v14 offset:1024
	ds_read_b128 v[10:13], v14 offset:2048
	ds_read_b128 v[14:17], v14 offset:3072
	ds_read_b128 v[18:21], v30
	ds_read_b128 v[22:25], v30 offset:1024
	ds_read_b128 v[26:29], v30 offset:2048
	ds_read_b128 v[30:33], v30 offset:3072
	s_mov_b32 m0, s50
	ds_read_b128 v[184:187], v183 offset:32768
	ds_read_b128 v[188:191], v183 offset:33792
	ds_read_b128 v[192:195], v183 offset:34816
	ds_read_b128 v[196:199], v183 offset:35840
	ds_read_b128 v[200:203], v183 offset:36864
	ds_read_b128 v[204:207], v183 offset:37888
	ds_read_b128 v[208:211], v183 offset:38912
	ds_read_b128 v[212:215], v183 offset:39936
	global_load_lds_dwordx4 v164, s[38:39]
	s_mov_b32 m0, s51
	s_nop 0
	global_load_lds_dwordx4 v162, s[38:39]
	s_waitcnt vmcnt(8) lgkmcnt(0)
	s_barrier
	s_setprio 1
	v_mfma_f32_16x16x128_f8f6f4 v[122:125], v[10:17], v[200:207], v[122:125]
	v_mfma_f32_16x16x128_f8f6f4 v[126:129], v[2:9], v[200:207], v[126:129]
	v_mfma_f32_16x16x128_f8f6f4 v[158:161], v[2:9], v[184:191], v[158:161]
	v_mfma_f32_16x16x128_f8f6f4 v[154:157], v[10:17], v[184:191], v[154:157]
	v_mfma_f32_16x16x128_f8f6f4 v[138:141], v[10:17], v[192:199], v[138:141]
	v_mfma_f32_16x16x128_f8f6f4 v[142:145], v[2:9], v[192:199], v[142:145]
	v_mfma_f32_16x16x128_f8f6f4 v[110:113], v[2:9], v[208:215], v[110:113]
	v_mfma_f32_16x16x128_f8f6f4 v[106:109], v[10:17], v[208:215], v[106:109]
	v_mfma_f32_16x16x128_f8f6f4 v[102:105], v[18:25], v[208:215], v[102:105]
	v_mfma_f32_16x16x128_f8f6f4 v[98:101], v[26:33], v[208:215], v[98:101]
	v_mfma_f32_16x16x128_f8f6f4 v[146:149], v[26:33], v[184:191], v[146:149]
	v_mfma_f32_16x16x128_f8f6f4 v[150:153], v[18:25], v[184:191], v[150:153]
	v_mfma_f32_16x16x128_f8f6f4 v[134:137], v[18:25], v[192:199], v[134:137]
	v_mfma_f32_16x16x128_f8f6f4 v[130:133], v[26:33], v[192:199], v[130:133]
	v_mfma_f32_16x16x128_f8f6f4 v[114:117], v[26:33], v[200:207], v[114:117]
	v_mfma_f32_16x16x128_f8f6f4 v[118:121], v[18:25], v[200:207], v[118:121]
	s_setprio 0
	s_barrier
	s_mov_b32 m0, s69
	v_lshl_add_u64 v[170:171], v[170:171], 0, s[8:9]
	ds_read_b128 v[184:187], v183 offset:49152
	ds_read_b128 v[188:191], v183 offset:50176
	ds_read_b128 v[192:195], v183 offset:51200
	ds_read_b128 v[196:199], v183 offset:52224
	ds_read_b128 v[200:203], v183 offset:53248
	ds_read_b128 v[204:207], v183 offset:54272
	ds_read_b128 v[208:211], v183 offset:55296
	ds_read_b128 v[212:215], v183 offset:56320
	global_load_lds_dwordx4 v[170:171], off
	v_lshl_add_u64 v[170:171], v[172:173], 0, s[8:9]
	s_mov_b32 m0, s67
	s_nop 0
	global_load_lds_dwordx4 v[170:171], off
	s_mov_b32 m0, s68
	s_nop 0
	global_load_lds_dwordx4 v164, s[36:37]
	s_mov_b32 m0, s66
	s_nop 0
	global_load_lds_dwordx4 v162, s[36:37]
	v_lshl_add_u64 v[170:171], v[174:175], 0, s[8:9]
	s_mov_b32 m0, s61
	s_nop 0
	global_load_lds_dwordx4 v[170:171], off
	v_lshl_add_u64 v[170:171], v[176:177], 0, s[8:9]
	s_mov_b32 m0, s62
	s_nop 0
	global_load_lds_dwordx4 v[170:171], off
	s_waitcnt vmcnt(8) lgkmcnt(0)
	s_barrier
	s_setprio 1
	v_mfma_f32_16x16x128_f8f6f4 v[62:65], v[2:9], v[200:207], v[62:65]
	v_mfma_f32_16x16x128_f8f6f4 v[58:61], v[10:17], v[200:207], v[58:61]
	v_mfma_f32_16x16x128_f8f6f4 v[90:93], v[10:17], v[184:191], v[90:93]
	v_mfma_f32_16x16x128_f8f6f4 v[94:97], v[2:9], v[184:191], v[94:97]
	v_mfma_f32_16x16x128_f8f6f4 v[78:81], v[2:9], v[192:199], v[78:81]
	v_mfma_f32_16x16x128_f8f6f4 v[74:77], v[10:17], v[192:199], v[74:77]
	v_mfma_f32_16x16x128_f8f6f4 v[42:45], v[10:17], v[208:215], v[42:45]
	v_mfma_f32_16x16x128_f8f6f4 v[54:57], v[2:9], v[208:215], v[54:57]
	v_mfma_f32_16x16x128_f8f6f4 v[38:41], v[18:25], v[208:215], v[38:41]
	v_mfma_f32_16x16x128_f8f6f4 v[34:37], v[26:33], v[208:215], v[34:37]
	v_mfma_f32_16x16x128_f8f6f4 v[82:85], v[26:33], v[184:191], v[82:85]
	v_mfma_f32_16x16x128_f8f6f4 v[86:89], v[18:25], v[184:191], v[86:89]
	v_mfma_f32_16x16x128_f8f6f4 v[70:73], v[18:25], v[192:199], v[70:73]
	v_mfma_f32_16x16x128_f8f6f4 v[66:69], v[26:33], v[192:199], v[66:69]
	v_mfma_f32_16x16x128_f8f6f4 v[46:49], v[26:33], v[200:207], v[46:49]
	v_mfma_f32_16x16x128_f8f6f4 v[50:53], v[18:25], v[200:207], v[50:53]
	s_setprio 0
	s_barrier
	s_movk_i32 s38, 0x100
	s_andn2_b64 vcc, exec, s[34:35]
	s_mov_b64 s[36:37], -1
	s_mov_b64 s[34:35], 0
	s_cbranch_vccz .LBB0_1558
	s_and_b64 vcc, exec, s[12:13]
	s_cbranch_vccz .LBB0_1561
	s_barrier

.LBB0_1745:
	s_add_u32 s8, s49, s6
	s_addc_u32 s9, s50, s7
	s_add_u32 s8, s8, 0x32800100
	s_addc_u32 s9, s9, 0
	s_add_u32 s73, s51, s6
	s_addc_u32 s74, s54, s7
	s_add_i32 s72, 0, 0x10000
	s_cmpk_eq_i32 s6, 0x2a00
	s_cselect_b32 s37, s5, s9
	s_cselect_b32 s36, s4, s8
	s_cselect_b32 s9, s13, s74
	s_cselect_b32 s8, s12, s73
	s_add_i32 s73, 0, 0x14000
	v_add_u32_e32 v2, s72, v188
	v_add_u32_e32 v6, s73, v188
	ds_read_b128 v[26:29], v2
	ds_read_b128 v[30:33], v2 offset:1024
	ds_read_b128 v[18:21], v2 offset:2048
	ds_read_b128 v[22:25], v2 offset:3072
	ds_read_b128 v[10:13], v6
	ds_read_b128 v[14:17], v6 offset:1024
	ds_read_b128 v[2:5], v6 offset:2048
	ds_read_b128 v[6:9], v6 offset:3072
	v_lshl_add_u64 v[214:215], v[168:169], 0, s[6:7]
	s_add_i32 m0, s64, 0xc000
	ds_read_b128 v[172:175], v189
	ds_read_b128 v[176:179], v189 offset:1024
	ds_read_b128 v[190:193], v189 offset:2048
	ds_read_b128 v[194:197], v189 offset:3072
	ds_read_b128 v[198:201], v189 offset:4096
	ds_read_b128 v[202:205], v189 offset:5120
	ds_read_b128 v[206:209], v189 offset:6144
	ds_read_b128 v[210:213], v189 offset:7168
	global_load_lds_dwordx4 v[214:215], off
	v_lshl_add_u64 v[214:215], v[170:171], 0, s[6:7]
	s_add_i32 m0, s64, 0xe000
	s_nop 0
	global_load_lds_dwordx4 v[214:215], off
	s_waitcnt vmcnt(8) lgkmcnt(0)
	s_barrier
	s_setprio 1
	v_mfma_f32_16x16x128_f8f6f4 v[158:161], v[26:33], v[172:179], v[158:161]
	v_mfma_f32_16x16x128_f8f6f4 v[154:157], v[18:25], v[172:179], v[154:157]
	v_mfma_f32_16x16x128_f8f6f4 v[118:121], v[18:25], v[190:197], v[118:121]
	v_mfma_f32_16x16x128_f8f6f4 v[122:125], v[26:33], v[190:197], v[122:125]
	v_mfma_f32_16x16x128_f8f6f4 v[126:129], v[26:33], v[198:205], v[126:129]
	v_mfma_f32_16x16x128_f8f6f4 v[114:117], v[18:25], v[198:205], v[114:117]
	v_mfma_f32_16x16x128_f8f6f4 v[106:109], v[18:25], v[206:213], v[106:109]
	v_mfma_f32_16x16x128_f8f6f4 v[110:113], v[26:33], v[206:213], v[110:113]
	v_mfma_f32_16x16x128_f8f6f4 v[102:105], v[10:17], v[206:213], v[102:105]
	v_mfma_f32_16x16x128_f8f6f4 v[98:101], v[2:9], v[206:213], v[98:101]
	v_mfma_f32_16x16x128_f8f6f4 v[146:149], v[2:9], v[172:179], v[146:149]
	v_mfma_f32_16x16x128_f8f6f4 v[150:153], v[10:17], v[172:179], v[150:153]
	v_mfma_f32_16x16x128_f8f6f4 v[142:145], v[10:17], v[190:197], v[142:145]
	v_mfma_f32_16x16x128_f8f6f4 v[138:141], v[2:9], v[190:197], v[138:141]
	v_mfma_f32_16x16x128_f8f6f4 v[130:133], v[2:9], v[198:205], v[130:133]
	v_mfma_f32_16x16x128_f8f6f4 v[134:137], v[10:17], v[198:205], v[134:137]
	s_setprio 0
	s_barrier
	s_add_i32 s72, s72, s43
	v_lshl_add_u64 v[172:173], s[8:9], 0, v[162:163]
	s_mov_b32 m0, s72
	ds_read_b128 v[190:193], v189 offset:16384
	ds_read_b128 v[194:197], v189 offset:17408
	ds_read_b128 v[198:201], v189 offset:18432
	ds_read_b128 v[202:205], v189 offset:19456
	ds_read_b128 v[206:209], v189 offset:20480
	ds_read_b128 v[210:213], v189 offset:21504
	ds_read_b128 v[214:217], v189 offset:22528
	ds_read_b128 v[218:221], v189 offset:23552
	global_load_lds_dwordx4 v[172:173], off
	s_add_i32 m0, s72, 0x2000
	s_add_u32 s74, s8, 0x158000
	v_lshl_add_u64 v[174:175], s[8:9], 0, v[166:167]
	s_addc_u32 s75, s9, 0
	s_add_i32 s72, s73, s43
	global_load_lds_dwordx4 v[174:175], off
	s_mov_b32 m0, s72
	v_lshl_add_u64 v[178:179], s[36:37], 0, v[166:167]
	global_load_lds_dwordx4 v162, s[74:75]
	s_add_i32 m0, s72, 0x2000
	s_nop 0
	global_load_lds_dwordx4 v166, s[74:75]
	v_lshl_add_u64 v[176:177], s[36:37], 0, v[162:163]
	s_mov_b32 m0, s64
	s_nop 0
	global_load_lds_dwordx4 v[176:177], off
	s_mov_b32 m0, s65
	s_nop 0
	global_load_lds_dwordx4 v[178:179], off
	s_waitcnt vmcnt(8) lgkmcnt(0)
	s_barrier
	s_setprio 1
	v_mfma_f32_16x16x128_f8f6f4 v[78:81], v[26:33], v[198:205], v[78:81]
	v_mfma_f32_16x16x128_f8f6f4 v[74:77], v[18:25], v[198:205], v[74:77]
	v_mfma_f32_16x16x128_f8f6f4 v[90:93], v[18:25], v[190:197], v[90:93]
	v_mfma_f32_16x16x128_f8f6f4 v[94:97], v[26:33], v[190:197], v[94:97]
	v_mfma_f32_16x16x128_f8f6f4 v[62:65], v[26:33], v[206:213], v[62:65]
	v_mfma_f32_16x16x128_f8f6f4 v[58:61], v[18:25], v[206:213], v[58:61]
	v_mfma_f32_16x16x128_f8f6f4 v[42:45], v[18:25], v[214:221], v[42:45]
	v_mfma_f32_16x16x128_f8f6f4 v[46:49], v[26:33], v[214:221], v[46:49]
	v_mfma_f32_16x16x128_f8f6f4 v[38:41], v[10:17], v[214:221], v[38:41]
	v_mfma_f32_16x16x128_f8f6f4 v[34:37], v[2:9], v[214:221], v[34:37]
	v_mfma_f32_16x16x128_f8f6f4 v[82:85], v[2:9], v[190:197], v[82:85]
	v_mfma_f32_16x16x128_f8f6f4 v[86:89], v[10:17], v[190:197], v[86:89]
	v_mfma_f32_16x16x128_f8f6f4 v[70:73], v[10:17], v[198:205], v[70:73]
	v_mfma_f32_16x16x128_f8f6f4 v[66:69], v[2:9], v[198:205], v[66:69]
	v_mfma_f32_16x16x128_f8f6f4 v[50:53], v[2:9], v[206:213], v[50:53]
	v_mfma_f32_16x16x128_f8f6f4 v[54:57], v[10:17], v[206:213], v[54:57]
	s_setprio 0
	s_barrier
	s_add_i32 s72, 0, 0x18000
	s_add_i32 s73, 0, 0x1c000
	v_add_u32_e32 v14, s72, v188
	v_add_u32_e32 v30, s73, v188
	ds_read_b128 v[2:5], v14
	ds_read_b128 v[6:9], v14 offset:1024
	ds_read_b128 v[10:13], v14 offset:2048
	ds_read_b128 v[14:17], v14 offset:3072
	ds_read_b128 v[18:21], v30
	ds_read_b128 v[22:25], v30 offset:1024
	ds_read_b128 v[26:29], v30 offset:2048
	ds_read_b128 v[30:33], v30 offset:3072
	s_add_u32 s36, s36, 0x158000
	s_addc_u32 s37, s37, 0
	s_mov_b32 m0, s66
	ds_read_b128 v[190:193], v189 offset:32768
	ds_read_b128 v[194:197], v189 offset:33792
	ds_read_b128 v[198:201], v189 offset:34816
	ds_read_b128 v[202:205], v189 offset:35840
	ds_read_b128 v[206:209], v189 offset:36864
	ds_read_b128 v[210:213], v189 offset:37888
	ds_read_b128 v[214:217], v189 offset:38912
	ds_read_b128 v[218:221], v189 offset:39936
	global_load_lds_dwordx4 v162, s[36:37]
	s_mov_b32 m0, s67
	s_nop 0
	global_load_lds_dwordx4 v166, s[36:37]
	s_waitcnt vmcnt(8) lgkmcnt(0)
	s_barrier
	s_setprio 1
	v_mfma_f32_16x16x128_f8f6f4 v[114:117], v[10:17], v[206:213], v[114:117]
	v_mfma_f32_16x16x128_f8f6f4 v[126:129], v[2:9], v[206:213], v[126:129]
	v_mfma_f32_16x16x128_f8f6f4 v[158:161], v[2:9], v[190:197], v[158:161]
	v_mfma_f32_16x16x128_f8f6f4 v[154:157], v[10:17], v[190:197], v[154:157]
	v_mfma_f32_16x16x128_f8f6f4 v[118:121], v[10:17], v[198:205], v[118:121]
	v_mfma_f32_16x16x128_f8f6f4 v[122:125], v[2:9], v[198:205], v[122:125]
	v_mfma_f32_16x16x128_f8f6f4 v[110:113], v[2:9], v[214:221], v[110:113]
	v_mfma_f32_16x16x128_f8f6f4 v[106:109], v[10:17], v[214:221], v[106:109]
	v_mfma_f32_16x16x128_f8f6f4 v[102:105], v[18:25], v[214:221], v[102:105]
	v_mfma_f32_16x16x128_f8f6f4 v[98:101], v[26:33], v[214:221], v[98:101]
	v_mfma_f32_16x16x128_f8f6f4 v[146:149], v[26:33], v[190:197], v[146:149]
	v_mfma_f32_16x16x128_f8f6f4 v[150:153], v[18:25], v[190:197], v[150:153]
	v_mfma_f32_16x16x128_f8f6f4 v[142:145], v[18:25], v[198:205], v[142:145]
	v_mfma_f32_16x16x128_f8f6f4 v[138:141], v[26:33], v[198:205], v[138:141]
	v_mfma_f32_16x16x128_f8f6f4 v[130:133], v[26:33], v[206:213], v[130:133]
	v_mfma_f32_16x16x128_f8f6f4 v[134:137], v[18:25], v[206:213], v[134:137]
	s_setprio 0
	s_barrier
	s_add_i32 s36, s72, s43
	v_lshl_add_u64 v[172:173], v[172:173], 0, s[22:23]
	s_mov_b32 m0, s36
	ds_read_b128 v[190:193], v189 offset:49152
	ds_read_b128 v[194:197], v189 offset:50176
	ds_read_b128 v[198:201], v189 offset:51200
	ds_read_b128 v[202:205], v189 offset:52224
	ds_read_b128 v[206:209], v189 offset:53248
	ds_read_b128 v[210:213], v189 offset:54272
	ds_read_b128 v[214:217], v189 offset:55296
	ds_read_b128 v[218:221], v189 offset:56320
	global_load_lds_dwordx4 v[172:173], off
	s_add_i32 m0, s36, 0x2000
	s_add_u32 s8, s8, 0x158080
	v_lshl_add_u64 v[172:173], v[174:175], 0, s[22:23]
	s_addc_u32 s9, s9, 0
	s_add_i32 s36, s73, s43
	global_load_lds_dwordx4 v[172:173], off
	s_mov_b32 m0, s36
	s_nop 0
	global_load_lds_dwordx4 v162, s[8:9]
	s_add_i32 m0, s36, 0x2000
	s_nop 0
	global_load_lds_dwordx4 v166, s[8:9]
	v_lshl_add_u64 v[172:173], v[176:177], 0, s[22:23]
	s_mov_b32 m0, s69
	s_nop 0
	global_load_lds_dwordx4 v[172:173], off
	v_lshl_add_u64 v[172:173], v[178:179], 0, s[22:23]
	s_mov_b32 m0, s70
	s_nop 0
	global_load_lds_dwordx4 v[172:173], off
	s_waitcnt vmcnt(8) lgkmcnt(0)
	s_barrier
	s_setprio 1
	v_mfma_f32_16x16x128_f8f6f4 v[62:65], v[2:9], v[206:213], v[62:65]
	v_mfma_f32_16x16x128_f8f6f4 v[58:61], v[10:17], v[206:213], v[58:61]
	v_mfma_f32_16x16x128_f8f6f4 v[90:93], v[10:17], v[190:197], v[90:93]
	v_mfma_f32_16x16x128_f8f6f4 v[94:97], v[2:9], v[190:197], v[94:97]
	v_mfma_f32_16x16x128_f8f6f4 v[78:81], v[2:9], v[198:205], v[78:81]
	v_mfma_f32_16x16x128_f8f6f4 v[74:77], v[10:17], v[198:205], v[74:77]
	v_mfma_f32_16x16x128_f8f6f4 v[42:45], v[10:17], v[214:221], v[42:45]
	v_mfma_f32_16x16x128_f8f6f4 v[46:49], v[2:9], v[214:221], v[46:49]
	v_mfma_f32_16x16x128_f8f6f4 v[38:41], v[18:25], v[214:221], v[38:41]
	v_mfma_f32_16x16x128_f8f6f4 v[34:37], v[26:33], v[214:221], v[34:37]
	v_mfma_f32_16x16x128_f8f6f4 v[82:85], v[26:33], v[190:197], v[82:85]
	v_mfma_f32_16x16x128_f8f6f4 v[86:89], v[18:25], v[190:197], v[86:89]
	v_mfma_f32_16x16x128_f8f6f4 v[70:73], v[18:25], v[198:205], v[70:73]
	v_mfma_f32_16x16x128_f8f6f4 v[66:69], v[26:33], v[198:205], v[66:69]
	v_mfma_f32_16x16x128_f8f6f4 v[50:53], v[26:33], v[206:213], v[50:53]
	v_mfma_f32_16x16x128_f8f6f4 v[54:57], v[18:25], v[206:213], v[54:57]
	s_setprio 0
	s_barrier
	s_add_i32 s71, s71, 2
	s_add_u32 s6, s6, 0x100
	s_addc_u32 s7, s7, 0
	s_cmpk_lt_u32 s71, 0x54
	s_cbranch_scc1 .LBB0_1745
	s_waitcnt vmcnt(0)
	s_cmpk_gt_u32 s40, 0xff
	s_cbranch_scc1 .LBB0_1748
	s_barrier

.LBB0_1807:
	ds_read_b128 v[26:29], v185
	ds_read_b128 v[30:33], v185 offset:1024
	ds_read_b128 v[18:21], v185 offset:2048
	ds_read_b128 v[22:25], v185 offset:3072
	ds_read_b128 v[10:13], v186
	ds_read_b128 v[14:17], v186 offset:1024
	ds_read_b128 v[2:5], v186 offset:2048
	ds_read_b128 v[6:9], v186 offset:3072
	s_add_u32 s28, s26, 0xffea8080
	s_addc_u32 s29, s27, -1
	s_cmpk_eq_i32 s58, 0x52
	s_cselect_b32 s31, s5, s29
	s_cselect_b32 s30, s4, s28
	s_cselect_b32 s29, s25, s57
	s_cselect_b32 s28, s24, s56
	s_add_i32 m0, s34, 0xc000
	ds_read_b128 v[174:177], v187
	ds_read_b128 v[178:181], v187 offset:1024
	ds_read_b128 v[188:191], v187 offset:2048
	ds_read_b128 v[192:195], v187 offset:3072
	ds_read_b128 v[196:199], v187 offset:4096
	ds_read_b128 v[200:203], v187 offset:5120
	ds_read_b128 v[204:207], v187 offset:6144
	ds_read_b128 v[208:211], v187 offset:7168
	global_load_lds_dwordx4 v166, s[26:27]
	v_lshl_add_u64 v[212:213], s[26:27], 0, v[168:169]
	s_add_i32 m0, s34, 0xe000
	s_nop 0
	global_load_lds_dwordx4 v[212:213], off
	s_waitcnt vmcnt(8) lgkmcnt(0)
	s_barrier
	s_setprio 1
	v_mfma_f32_16x16x128_f8f6f4 v[158:161], v[26:33], v[174:181], v[158:161]
	v_mfma_f32_16x16x128_f8f6f4 v[154:157], v[18:25], v[174:181], v[154:157]
	v_mfma_f32_16x16x128_f8f6f4 v[138:141], v[18:25], v[188:195], v[138:141]
	v_mfma_f32_16x16x128_f8f6f4 v[142:145], v[26:33], v[188:195], v[142:145]
	v_mfma_f32_16x16x128_f8f6f4 v[126:129], v[26:33], v[196:203], v[126:129]
	v_mfma_f32_16x16x128_f8f6f4 v[122:125], v[18:25], v[196:203], v[122:125]
	v_mfma_f32_16x16x128_f8f6f4 v[106:109], v[18:25], v[204:211], v[106:109]
	v_mfma_f32_16x16x128_f8f6f4 v[110:113], v[26:33], v[204:211], v[110:113]
	v_mfma_f32_16x16x128_f8f6f4 v[102:105], v[10:17], v[204:211], v[102:105]
	v_mfma_f32_16x16x128_f8f6f4 v[98:101], v[2:9], v[204:211], v[98:101]
	v_mfma_f32_16x16x128_f8f6f4 v[146:149], v[2:9], v[174:181], v[146:149]
	v_mfma_f32_16x16x128_f8f6f4 v[150:153], v[10:17], v[174:181], v[150:153]
	v_mfma_f32_16x16x128_f8f6f4 v[134:137], v[10:17], v[188:195], v[134:137]
	v_mfma_f32_16x16x128_f8f6f4 v[130:133], v[2:9], v[188:195], v[130:133]
	v_mfma_f32_16x16x128_f8f6f4 v[114:117], v[2:9], v[196:203], v[114:117]
	v_mfma_f32_16x16x128_f8f6f4 v[118:121], v[10:17], v[196:203], v[118:121]
	s_setprio 0
	s_barrier
	s_add_i32 s59, s42, s3
	v_lshl_add_u64 v[174:175], s[28:29], 0, v[164:165]
	s_mov_b32 m0, s59
	ds_read_b128 v[188:191], v187 offset:16384
	ds_read_b128 v[192:195], v187 offset:17408
	ds_read_b128 v[196:199], v187 offset:18432
	ds_read_b128 v[200:203], v187 offset:19456
	ds_read_b128 v[204:207], v187 offset:20480
	ds_read_b128 v[208:211], v187 offset:21504
	ds_read_b128 v[212:215], v187 offset:22528
	ds_read_b128 v[216:219], v187 offset:23552
	global_load_lds_dwordx4 v[174:175], off
	s_add_i32 m0, s59, 0x2000
	s_add_u32 s60, s28, 0x158000
	v_lshl_add_u64 v[176:177], s[28:29], 0, v[162:163]
	s_addc_u32 s61, s29, 0
	s_add_i32 s59, s43, s3
	global_load_lds_dwordx4 v[176:177], off
	s_mov_b32 m0, s59
	v_lshl_add_u64 v[180:181], s[30:31], 0, v[162:163]
	global_load_lds_dwordx4 v164, s[60:61]
	s_add_i32 m0, s59, 0x2000
	s_nop 0
	global_load_lds_dwordx4 v162, s[60:61]
	v_lshl_add_u64 v[178:179], s[30:31], 0, v[164:165]
	s_mov_b32 m0, s34
	s_nop 0
	global_load_lds_dwordx4 v[178:179], off
	s_mov_b32 m0, s35
	s_nop 0
	global_load_lds_dwordx4 v[180:181], off
	s_waitcnt vmcnt(8) lgkmcnt(0)
	s_barrier
	s_setprio 1
	v_mfma_f32_16x16x128_f8f6f4 v[78:81], v[26:33], v[196:203], v[78:81]
	v_mfma_f32_16x16x128_f8f6f4 v[74:77], v[18:25], v[196:203], v[74:77]
	v_mfma_f32_16x16x128_f8f6f4 v[90:93], v[18:25], v[188:195], v[90:93]
	v_mfma_f32_16x16x128_f8f6f4 v[94:97], v[26:33], v[188:195], v[94:97]
	v_mfma_f32_16x16x128_f8f6f4 v[62:65], v[26:33], v[204:211], v[62:65]
	v_mfma_f32_16x16x128_f8f6f4 v[58:61], v[18:25], v[204:211], v[58:61]
	v_mfma_f32_16x16x128_f8f6f4 v[42:45], v[18:25], v[212:219], v[42:45]
	v_mfma_f32_16x16x128_f8f6f4 v[54:57], v[26:33], v[212:219], v[54:57]
	v_mfma_f32_16x16x128_f8f6f4 v[38:41], v[10:17], v[212:219], v[38:41]
	v_mfma_f32_16x16x128_f8f6f4 v[34:37], v[2:9], v[212:219], v[34:37]
	v_mfma_f32_16x16x128_f8f6f4 v[82:85], v[2:9], v[188:195], v[82:85]
	v_mfma_f32_16x16x128_f8f6f4 v[86:89], v[10:17], v[188:195], v[86:89]
	v_mfma_f32_16x16x128_f8f6f4 v[70:73], v[10:17], v[196:203], v[70:73]
	v_mfma_f32_16x16x128_f8f6f4 v[66:69], v[2:9], v[196:203], v[66:69]
	v_mfma_f32_16x16x128_f8f6f4 v[46:49], v[2:9], v[204:211], v[46:49]
	v_mfma_f32_16x16x128_f8f6f4 v[50:53], v[10:17], v[204:211], v[50:53]
	s_setprio 0
	s_barrier
	s_add_i32 s59, 0, 0x18000
	s_add_i32 s60, 0, 0x1c000
	v_add_u32_e32 v14, s59, v183
	v_add_u32_e32 v30, s60, v183
	ds_read_b128 v[2:5], v14
	ds_read_b128 v[6:9], v14 offset:1024
	ds_read_b128 v[10:13], v14 offset:2048
	ds_read_b128 v[14:17], v14 offset:3072
	ds_read_b128 v[18:21], v30
	ds_read_b128 v[22:25], v30 offset:1024
	ds_read_b128 v[26:29], v30 offset:2048
	ds_read_b128 v[30:33], v30 offset:3072
	s_add_u32 s30, s30, 0x158000
	s_addc_u32 s31, s31, 0
	s_mov_b32 m0, s36
	ds_read_b128 v[188:191], v187 offset:32768
	ds_read_b128 v[192:195], v187 offset:33792
	ds_read_b128 v[196:199], v187 offset:34816
	ds_read_b128 v[200:203], v187 offset:35840
	ds_read_b128 v[204:207], v187 offset:36864
	ds_read_b128 v[208:211], v187 offset:37888
	ds_read_b128 v[212:215], v187 offset:38912
	ds_read_b128 v[216:219], v187 offset:39936
	global_load_lds_dwordx4 v164, s[30:31]
	s_mov_b32 m0, s37
	s_nop 0
	global_load_lds_dwordx4 v162, s[30:31]
	s_waitcnt vmcnt(8) lgkmcnt(0)
	s_barrier
	s_setprio 1
	v_mfma_f32_16x16x128_f8f6f4 v[122:125], v[10:17], v[204:211], v[122:125]
	v_mfma_f32_16x16x128_f8f6f4 v[126:129], v[2:9], v[204:211], v[126:129]
	v_mfma_f32_16x16x128_f8f6f4 v[158:161], v[2:9], v[188:195], v[158:161]
	v_mfma_f32_16x16x128_f8f6f4 v[154:157], v[10:17], v[188:195], v[154:157]
	v_mfma_f32_16x16x128_f8f6f4 v[138:141], v[10:17], v[196:203], v[138:141]
	v_mfma_f32_16x16x128_f8f6f4 v[142:145], v[2:9], v[196:203], v[142:145]
	v_mfma_f32_16x16x128_f8f6f4 v[110:113], v[2:9], v[212:219], v[110:113]
	v_mfma_f32_16x16x128_f8f6f4 v[106:109], v[10:17], v[212:219], v[106:109]
	v_mfma_f32_16x16x128_f8f6f4 v[102:105], v[18:25], v[212:219], v[102:105]
	v_mfma_f32_16x16x128_f8f6f4 v[98:101], v[26:33], v[212:219], v[98:101]
	v_mfma_f32_16x16x128_f8f6f4 v[146:149], v[26:33], v[188:195], v[146:149]
	v_mfma_f32_16x16x128_f8f6f4 v[150:153], v[18:25], v[188:195], v[150:153]
	v_mfma_f32_16x16x128_f8f6f4 v[134:137], v[18:25], v[196:203], v[134:137]
	v_mfma_f32_16x16x128_f8f6f4 v[130:133], v[26:33], v[196:203], v[130:133]
	v_mfma_f32_16x16x128_f8f6f4 v[114:117], v[26:33], v[204:211], v[114:117]
	v_mfma_f32_16x16x128_f8f6f4 v[118:121], v[18:25], v[204:211], v[118:121]
	s_setprio 0
	s_barrier
	s_add_i32 s30, s59, s3
	v_lshl_add_u64 v[174:175], v[174:175], 0, s[10:11]
	s_mov_b32 m0, s30
	ds_read_b128 v[188:191], v187 offset:49152
	ds_read_b128 v[192:195], v187 offset:50176
	ds_read_b128 v[196:199], v187 offset:51200
	ds_read_b128 v[200:203], v187 offset:52224
	ds_read_b128 v[204:207], v187 offset:53248
	ds_read_b128 v[208:211], v187 offset:54272
	ds_read_b128 v[212:215], v187 offset:55296
	ds_read_b128 v[216:219], v187 offset:56320
	global_load_lds_dwordx4 v[174:175], off
	s_add_i32 m0, s30, 0x2000
	s_add_u32 s28, s28, 0x158080
	v_lshl_add_u64 v[174:175], v[176:177], 0, s[10:11]
	s_addc_u32 s29, s29, 0
	s_add_i32 s30, s60, s3
	global_load_lds_dwordx4 v[174:175], off
	s_mov_b32 m0, s30
	s_nop 0
	global_load_lds_dwordx4 v164, s[28:29]
	s_add_i32 m0, s30, 0x2000
	s_nop 0
	global_load_lds_dwordx4 v162, s[28:29]
	v_lshl_add_u64 v[174:175], v[178:179], 0, s[10:11]
	s_mov_b32 m0, s40
	s_nop 0
	global_load_lds_dwordx4 v[174:175], off
	v_lshl_add_u64 v[174:175], v[180:181], 0, s[10:11]
	s_mov_b32 m0, s41
	s_nop 0
	global_load_lds_dwordx4 v[174:175], off
	s_waitcnt vmcnt(8) lgkmcnt(0)
	s_barrier
	s_setprio 1
	v_mfma_f32_16x16x128_f8f6f4 v[62:65], v[2:9], v[204:211], v[62:65]
	v_mfma_f32_16x16x128_f8f6f4 v[58:61], v[10:17], v[204:211], v[58:61]
	v_mfma_f32_16x16x128_f8f6f4 v[90:93], v[10:17], v[188:195], v[90:93]
	v_mfma_f32_16x16x128_f8f6f4 v[94:97], v[2:9], v[188:195], v[94:97]
	v_mfma_f32_16x16x128_f8f6f4 v[78:81], v[2:9], v[196:203], v[78:81]
	v_mfma_f32_16x16x128_f8f6f4 v[74:77], v[10:17], v[196:203], v[74:77]
	v_mfma_f32_16x16x128_f8f6f4 v[42:45], v[10:17], v[212:219], v[42:45]
	v_mfma_f32_16x16x128_f8f6f4 v[54:57], v[2:9], v[212:219], v[54:57]
	v_mfma_f32_16x16x128_f8f6f4 v[38:41], v[18:25], v[212:219], v[38:41]
	v_mfma_f32_16x16x128_f8f6f4 v[34:37], v[26:33], v[212:219], v[34:37]
	v_mfma_f32_16x16x128_f8f6f4 v[82:85], v[26:33], v[188:195], v[82:85]
	v_mfma_f32_16x16x128_f8f6f4 v[86:89], v[18:25], v[188:195], v[86:89]
	v_mfma_f32_16x16x128_f8f6f4 v[70:73], v[18:25], v[196:203], v[70:73]
	v_mfma_f32_16x16x128_f8f6f4 v[66:69], v[26:33], v[196:203], v[66:69]
	v_mfma_f32_16x16x128_f8f6f4 v[46:49], v[26:33], v[204:211], v[46:49]
	v_mfma_f32_16x16x128_f8f6f4 v[50:53], v[18:25], v[204:211], v[50:53]
	s_setprio 0
	s_barrier
	s_add_i32 s58, s58, 2
	s_add_u32 s26, s26, 0x100
	s_addc_u32 s27, s27, 0
	s_add_u32 s56, s56, 0x100
	s_addc_u32 s57, s57, 0
	s_cmpk_gt_u32 s58, 0x53
	s_cbranch_scc0 .LBB0_1807
	s_and_b64 vcc, exec, s[12:13]
	s_cbranch_vccz .LBB0_1810
	s_barrier
